# combo: late drain in expert loops + de-serialized gate/up prologue list loads + removed redundant store waits in gate/up epilogue + hoisted bias loads in down epilogue
# speedup vs baseline: 1.0154x; 1.0154x over previous
; __device__ __forceinline__ int tid_opaque() { int t = threadIdx.x; asm volatile("" : "+v"(t)); return t; }
; __device__ __forceinline__ __amdgpu_buffer_rsrc_t mk_rsrc(const void* p) { return __builtin_amdgcn_make_buffer_rsrc((void*)p, 0, 0x7ffffff0, 0x00020000); }
;     __device__ __forceinline__ void init() {
;         const int tid = tid_opaque(), wid = tid >> 6, lane = tid & 63;
;         wr = wid >> 2; wc = wid & 3; fr = lane & 15; fq = lane >> 4;
;         aR = (wid >> 1) * 16 + (lane >> 2); aC = (wid & 1) * 32 + (((lane & 3) ^ ((lane >> 5) << 1)) * 8);
;         a_w = (unsigned)(wid * 1024 + lane * 16);
;         { const int l32 = lane & 31, kc8 = 2 * (wid >> 1) + (lane >> 5), wc_ = l32 >> 3, bfq = (l32 >> 1) & 3, nlo = l32 & 1; b_p = wid & 1;
;           b_k = kc8 * 8; b_col = wc_ * 64 + b_p * 32 + bfq * 8 + nlo * 4; b_gucol = wc_ * 32 + bfq * 8 + nlo * 4;
;           const int sub = wc_ * 4 + 2 * b_p + nlo;
;           b_w = (unsigned)((sub * 2 + (kc8 >> 2)) * 1024 + (((4 * bfq) * 64 + (kc8 & 3) * 16) ^ ((bfq >> 1) << 5))); b_rot = (unsigned)(nlo * 64); }
;         const unsigned lo = (unsigned)((fr * 64 + fq * 16) ^ ((fr >> 3) << 5));
;         a_r = (unsigned)(wr * 16384) + lo; b_r = 32768u + (unsigned)(wc * 8192) + lo;
; __device__ __forceinline__ void phase_moe_gu(const Ptrs& p, LAS unsigned char* lds) {
;     ...
;         const int* list = (const int*)(p.ws + OFF_LIST) + (size_t)mu.e * NTOK; const int i0 = mu.mt * 256, n0 = mu.nt * 128;
;         unsigned ao[4];
; #pragma unroll
;         for (int i = 0; i < 4; ++i) { const int r = i0 + T.aR + 64 * i; const int tok = (r < mu.cnt) ? (list[r] >> 2) : 0; ao[i] = (unsigned)((tok * D + T.aC) * 2); }
;         const float* wsel = ((__builtin_amdgcn_readfirstlane(T.b_p) & 1) ? p.w_up : p.w_gate) + (size_t)mu.e * D * D + n0;
;         const unsigned bo = (unsigned)((T.b_k * D + T.b_gucol) * 4);
;         f32x4 acc[8][4]; acc_zero(acc);
;         const int mlim = __builtin_amdgcn_readfirstlane(T.wr) ? 0 : ((mu.cnt - i0 + 15) >> 4);
;         if (mu.light) gemm_kloop_light(acc, lds, T, mk_rsrc(h2), ao[0], ao[1], ao[2], ao[3], mk_rsrc(wsel), bo, D * 4u, D / 64, mlim);
.LBB0_1163:
	s_andn2_b64 vcc, exec, s[0:1]
	s_mov_b64 s[0:1], -1
	s_cbranch_vccnz .LBB0_1005
	s_ashr_i32 s43, s42, 31
	s_lshl_b64 s[0:1], s[42:43], 15
	v_mov_b32_e32 v3, v0
	s_add_u32 s0, s52, s0
	s_addc_u32 s1, s53, s1
	v_bfe_u32 v4, v3, 2, 4
	s_lshl_b32 s2, s86, 8
	v_ashrrev_i32_e32 v10, 7, v3
	v_or_b32_e32 v4, s2, v4
	v_lshl_add_u32 v4, v10, 4, v4
	v_cmp_gt_i32_e32 vcc, s87, v4
	v_mov_b32_e32 v6, 0
	v_ashrrev_i32_e32 v5, 31, v4
	v_mov_b32_e32 v7, 0
	v_mov_b32_e32 v8, 0
	v_mov_b32_e32 v9, 0
	v_lshl_add_u64 v[12:13], v[4:5], 2, s[0:1]
	s_and_saveexec_b64 s[4:5], vcc
	global_load_dword v7, v[12:13], off
	s_or_b64 exec, exec, s[4:5]
	v_add_u32_e32 v11, 64, v4
	v_cmp_gt_i32_e32 vcc, s87, v11
	s_and_saveexec_b64 s[4:5], vcc
	global_load_dword v6, v[12:13], off offset:256
	s_or_b64 exec, exec, s[4:5]
	v_add_u32_e32 v11, 0x80, v4
	v_cmp_gt_i32_e32 vcc, s87, v11
	s_and_saveexec_b64 s[4:5], vcc
	global_load_dword v9, v[12:13], off offset:512
	s_or_b64 exec, exec, s[4:5]
	v_add_u32_e32 v11, 0xc0, v4
	v_cmp_gt_i32_e32 vcc, s87, v11
	s_and_saveexec_b64 s[4:5], vcc
	global_load_dword v8, v[12:13], off offset:768
	s_or_b64 exec, exec, s[4:5]
	v_ashrrev_i32_e32 v5, 6, v3
	v_and_b32_e32 v11, 1, v5
	s_lshl_b32 s0, s85, 7
	v_readfirstlane_b32 s1, v11
	v_readlane_b32 s4, v246, 0
	s_bitcmp0_b32 s1, 0
	v_readlane_b32 s5, v246, 1
	s_cselect_b32 s1, s49, s5
	s_cselect_b32 s3, s48, s4
	s_lshl_b64 s[4:5], s[42:43], 24
	v_readlane_b32 s6, v246, 2
	s_add_u32 s3, s3, s4
	v_and_b32_e32 v4, 63, v3
	s_addc_u32 s6, s1, s5
	s_ashr_i32 s1, s0, 31
	v_lshrrev_b32_e32 v12, 5, v4
	v_bfe_u32 v13, v3, 1, 2
	s_lshl_b64 s[4:5], s[0:1], 2
	v_lshl_or_b32 v10, v10, 1, v12
	v_bfe_u32 v12, v3, 3, 2
	v_and_b32_e32 v14, 1, v3
	v_lshlrev_b32_e32 v15, 5, v13
	s_add_u32 s24, s3, s4
	v_lshl_or_b32 v15, v12, 7, v15
	v_lshlrev_b32_e32 v16, 16, v10
	v_lshlrev_b32_e32 v17, 4, v14
	s_addc_u32 s1, s6, s5
	v_or3_b32 v225, v15, v17, v16
	s_and_b32 s25, s1, 0xffff
	s_movk_i32 s1, 0x2000
	buffer_load_dwordx4 v[114:117], v225, s[24:27], 0 offen
	buffer_load_dwordx4 v[118:121], v225, s[24:27], s66 offen
	s_mov_b32 s3, 0x8000
	buffer_load_dwordx4 v[126:129], v225, s[24:27], s1 offen
	buffer_load_dwordx4 v[122:125], v225, s[24:27], s3 offen
	s_movk_i32 s1, 0x4000
	s_mov_b32 s3, 0xa000
	buffer_load_dwordx4 v[130:133], v225, s[24:27], s1 offen
	buffer_load_dwordx4 v[134:137], v225, s[24:27], s3 offen
	s_mov_b32 s1, 0xc000
	s_mov_b32 s3, 0xe000
	buffer_load_dwordx4 v[142:145], v225, s[24:27], s1 offen
	buffer_load_dwordx4 v[146:149], v225, s[24:27], s3 offen
	s_waitcnt vmcnt(8)
	v_lshlrev_b32_e32 v7, 10, v7
	v_and_b32_e32 v7, 0xfffff000, v7
	v_lshlrev_b32_e32 v6, 10, v6
	v_and_b32_e32 v6, 0xfffff000, v6
	v_lshlrev_b32_e32 v9, 10, v9
	v_and_b32_e32 v9, 0xfffff000, v9
	v_lshlrev_b32_e32 v8, 10, v8
	v_and_b32_e32 v8, 0xfffff000, v8
	v_lshlrev_b32_e32 v17, 4, v3
	v_lshlrev_b32_e32 v15, 6, v11
	v_and_b32_e32 v16, 32, v3
	v_and_b32_e32 v17, 48, v17
	v_bitop3_b32 v15, v17, v15, v16 bitop3:0xde
	v_or_b32_e32 v221, v9, v15
	v_lshlrev_b32_e32 v9, 2, v12
	v_lshlrev_b32_e32 v11, 1, v11
	v_or3_b32 v9, v9, v11, v14
	v_lshlrev_b32_e32 v11, 2, v3
	v_and_b32_e32 v12, 0xfffffc00, v11
	v_lshl_add_u32 v9, v9, 11, v12
	v_lshlrev_b32_e32 v12, 8, v13
	v_lshlrev_b32_e32 v10, 4, v10
	v_and_or_b32 v10, v10, 48, v12
	v_lshlrev_b32_e32 v12, 3, v3
	v_or_b32_e32 v223, v7, v15
	v_and_b32_e32 v7, 15, v3
	v_and_b32_e32 v12, 32, v12
	v_or_b32_e32 v222, v6, v15
	v_ashrrev_i32_e32 v6, 8, v3
	v_bitop3_b32 v219, v9, v10, v12 bitop3:0xf6
	v_lshlrev_b32_e32 v7, 6, v7
	v_and_b32_e32 v3, 48, v3
	v_and_b32_e32 v10, 32, v11
	v_or_b32_e32 v9, v7, v3
	v_bitop3_b32 v3, v7, v10, v3 bitop3:0x36
	v_lshlrev_b32_e32 v11, 13, v5
	v_lshlrev_b32_e32 v220, 6, v14
	v_lshlrev_b32_e32 v4, 4, v4
	v_lshlrev_b32_e32 v7, 14, v6
	v_and_or_b32 v226, v11, s66, v3
	v_cmp_eq_u32_e32 vcc, 0, v215
	v_add_u32_e32 v227, 0, v219
	v_add_u32_e32 v3, 0xc0, v220
	v_or_b32_e32 v224, v8, v15
	v_lshl_or_b32 v229, v5, 10, v4
	v_bitop3_b32 v216, v9, v7, v10 bitop3:0xde
	v_or_b32_e32 v217, 0x8000, v226
	v_readfirstlane_b32 s1, v6
	s_and_b64 vcc, exec, vcc
	v_add_u32_e32 v228, v227, v220
	v_and_b32_e32 v218, 0xc0, v3
	v_readlane_b32 s7, v246, 3
	v_readlane_b32 s8, v246, 4
	v_readlane_b32 s9, v246, 5
	v_readlane_b32 s10, v246, 6
	v_readlane_b32 s11, v246, 7
	s_cbranch_vccnz .LBB0_1263
; #define LAS __attribute__((address_space(3)))
; #define G_DMA_A(buf, t, i_) __builtin_amdgcn_raw_ptr_buffer_load_lds(ra, (LAS void*)(lds + (buf) * 65536 + a_wu + (i_) * 8192), 16, ao##i_, (unsigned)(t) * 128u, 0, 0)
; #define G_ISSUE_B(t) do { const unsigned so_ = (unsigned)(t) * 64u * ldbB; _Pragma("unroll") for (int i_ = 0; i_ < 8; ++i_) sb[i_] = __builtin_bit_cast(f32x4, __builtin_amdgcn_raw_buffer_load_b128(rb, bo, so_ + (unsigned)i_ * ldbB, 0)); } while (0)
; #define G_RETIRE() asm volatile("s_waitcnt vmcnt(0)" : "+v"(sb[0]), "+v"(sb[1]), "+v"(sb[2]), "+v"(sb[3]), "+v"(sb[4]), "+v"(sb[5]), "+v"(sb[6]), "+v"(sb[7]) :: "memory")
; #define G_WRITE_B(buf) do { LAS unsigned char* d_ = lds + (buf) * 65536; \
;         _Pragma("unroll") for (int j_ = 0; j_ < 4; ++j_) { u32x4 w_; w_.x = cvtpk(sb[0][j_], sb[1][j_]); w_.y = cvtpk(sb[2][j_], sb[3][j_]); w_.z = cvtpk(sb[4][j_], sb[5][j_]); w_.w = cvtpk(sb[6][j_], sb[7][j_]); \
;             *(LAS u32x4*)(d_ + 32768 + T.b_w + ((T.b_rot + 64u * j_) & 255u)) = w_; } } while (0)
; #define G_BAR() do { asm volatile("s_waitcnt lgkmcnt(0)" ::: "memory"); __builtin_amdgcn_s_barrier(); asm volatile("" ::: "memory"); } while (0)
; __device__ __forceinline__ void gemm_kloop_light(f32x4 (&acc)[8][4], LAS unsigned char* lds, const GemmT& T, ...
;     ...
;     G_ISSUE_B(0); G_DMA_A(0, 0, 0); G_DMA_A(0, 0, 1); G_DMA_A(0, 0, 2); G_DMA_A(0, 0, 3); G_RETIRE(); G_WRITE_B(0);
;     if (nt > 1) G_ISSUE_B(1);
;     G_BAR();
;     for (int t = 0; t < nt; ++t) { const int cur = t & 1; const bool w1 = t + 1 < nt, i2 = t + 2 < nt;
;         if (w1) { G_DMA_A(cur ^ 1, t + 1, 0); G_DMA_A(cur ^ 1, t + 1, 1); G_DMA_A(cur ^ 1, t + 1, 2); G_DMA_A(cur ^ 1, t + 1, 3); }
;         if (mlim > 0) {
; #pragma unroll
;             for (int ks = 0; ks < 2; ++ks) { const LAS unsigned char* s_ = lds + cur * 65536 + ks * 1024; bf16x8 Bf_[4];
; #pragma unroll
;                 for (int n_ = 0; n_ < 4; ++n_) Bf_[n_] = *(const LAS bf16x8*)(s_ + T.b_r + n_ * 2048);
; #pragma unroll
;                 for (int m_ = 0; m_ < 8; ++m_) if (m_ < mlim) { const bf16x8 At_ = *(const LAS bf16x8*)(s_ + T.a_r + m_ * 2048);
; __device__ __forceinline__ void phase_moe_gu(const Ptrs& p, LAS unsigned char* lds) {
;     ...
;         const int mlim = __builtin_amdgcn_readfirstlane(T.wr) ? 0 : ((mu.cnt - i0 + 15) >> 4);
	s_sub_i32 s3, s87, s2
	s_add_i32 s3, s3, 15
	s_ashr_i32 s3, s3, 4
	s_cmp_eq_u32 s1, 0
	s_cselect_b32 s1, s3, 0
	v_readfirstlane_b32 s3, v229
	s_and_b32 s3, s3, 0xfffffc00
	s_add_i32 s3, s3, 0
	s_mov_b32 s38, s26
	s_mov_b32 s39, s27
	s_mov_b32 m0, s3
	s_waitcnt vmcnt(6)
	v_mov_b64_e32 v[4:5], v[118:119]
	buffer_load_dwordx4 v223, s[36:39], 0 offen lds
	s_add_i32 m0, s3, 0x2000
	s_waitcnt vmcnt(3)
	v_mov_b64_e32 v[8:9], v[134:135]
	buffer_load_dwordx4 v222, s[36:39], 0 offen lds
	s_add_i32 m0, s3, 0x4000
	v_mov_b64_e32 v[12:13], v[114:115]
	buffer_load_dwordx4 v221, s[36:39], 0 offen lds
	s_add_i32 m0, s3, 0x6000
	s_waitcnt vmcnt(3)
	v_mov_b64_e32 v[16:17], v[146:147]
	v_mov_b64_e32 v[20:21], v[130:131]
	v_mov_b64_e32 v[24:25], v[122:123]
	v_mov_b64_e32 v[28:29], v[142:143]
	v_mov_b64_e32 v[32:33], v[126:127]
	buffer_load_dwordx4 v224, s[36:39], 0 offen lds
	v_mov_b64_e32 v[6:7], v[120:121]
	v_mov_b64_e32 v[10:11], v[136:137]
	v_mov_b64_e32 v[14:15], v[116:117]
	v_mov_b64_e32 v[18:19], v[148:149]
	v_mov_b64_e32 v[22:23], v[132:133]
	v_mov_b64_e32 v[26:27], v[124:125]
	v_mov_b64_e32 v[30:31], v[144:145]
	v_mov_b64_e32 v[34:35], v[128:129]
	s_waitcnt vmcnt(0)
	buffer_load_dwordx4 v[162:165], v225, s[24:27], s67 offen
	buffer_load_dwordx4 v[166:169], v225, s[24:27], s76 offen
	buffer_load_dwordx4 v[170:173], v225, s[24:27], s77 offen
	buffer_load_dwordx4 v[174:177], v225, s[24:27], s78 offen
	buffer_load_dwordx4 v[178:181], v225, s[24:27], s79 offen
	buffer_load_dwordx4 v[182:185], v225, s[24:27], s80 offen
	buffer_load_dwordx4 v[186:189], v225, s[24:27], s81 offen
	buffer_load_dwordx4 v[190:193], v225, s[24:27], s82 offen
	s_cmp_gt_i32 s1, 0
	s_cselect_b64 s[62:63], -1, 0
	s_cmp_lg_u32 s1, 1
	v_cvt_pk_bf16_f32 v36, v12, v32
	v_cvt_pk_bf16_f32 v37, v20, v4
	v_cvt_pk_bf16_f32 v38, v24, v8
	v_cvt_pk_bf16_f32 v39, v28, v16
	s_cselect_b64 s[60:61], -1, 0
	s_cmp_gt_i32 s1, 2
	ds_write_b128 v228, v[36:39] offset:32768
	v_cvt_pk_bf16_f32 v36, v13, v33
	v_cvt_pk_bf16_f32 v37, v21, v5
	v_cvt_pk_bf16_f32 v38, v25, v9
	v_cvt_pk_bf16_f32 v39, v29, v17
	s_cselect_b64 s[58:59], -1, 0
	s_cmp_gt_i32 s1, 3
	ds_write_b128 v228, v[36:39] offset:32832
	v_cvt_pk_bf16_f32 v36, v14, v34
	v_cvt_pk_bf16_f32 v37, v22, v6
	v_cvt_pk_bf16_f32 v38, v26, v10
	v_cvt_pk_bf16_f32 v39, v30, v18
	v_cvt_pk_bf16_f32 v4, v15, v35
	v_cvt_pk_bf16_f32 v5, v23, v7
	v_cvt_pk_bf16_f32 v6, v27, v11
	v_cvt_pk_bf16_f32 v7, v31, v19
	v_add_u32_e32 v3, v227, v218
	s_cselect_b64 s[54:55], -1, 0
	s_cmp_gt_i32 s1, 4
	ds_write_b128 v228, v[36:39] offset:32896
	ds_write_b128 v3, v[4:7] offset:32768
	s_cselect_b64 s[46:47], -1, 0
	s_cmp_gt_i32 s1, 5
	s_waitcnt lgkmcnt(0)
	s_barrier
	s_cselect_b64 s[44:45], -1, 0
	s_cmp_gt_i32 s1, 6
	v_mov_b32_e32 v4, v2
	v_mov_b32_e32 v5, v2
	s_cselect_b64 s[34:35], -1, 0
	s_cmp_gt_i32 s1, 7
	v_mov_b32_e32 v3, v2
	v_mov_b64_e32 v[16:17], v[4:5]
	v_mov_b64_e32 v[8:9], v[4:5]
	v_mov_b64_e32 v[20:21], v[4:5]
	v_mov_b64_e32 v[12:13], v[4:5]
	v_mov_b64_e32 v[32:33], v[4:5]
	v_mov_b64_e32 v[24:25], v[4:5]
	v_mov_b64_e32 v[36:37], v[4:5]
	v_mov_b64_e32 v[28:29], v[4:5]
	v_mov_b64_e32 v[48:49], v[4:5]
	v_mov_b64_e32 v[40:41], v[4:5]
	v_mov_b64_e32 v[52:53], v[4:5]
	v_mov_b64_e32 v[44:45], v[4:5]
	v_mov_b64_e32 v[64:65], v[4:5]
	v_mov_b64_e32 v[56:57], v[4:5]
	v_mov_b64_e32 v[68:69], v[4:5]
	v_mov_b64_e32 v[60:61], v[4:5]
	v_mov_b64_e32 v[80:81], v[4:5]
	v_mov_b64_e32 v[72:73], v[4:5]
	v_mov_b64_e32 v[84:85], v[4:5]
	v_mov_b64_e32 v[76:77], v[4:5]
	v_mov_b64_e32 v[96:97], v[4:5]
	v_mov_b64_e32 v[88:89], v[4:5]
	v_mov_b64_e32 v[100:101], v[4:5]
	v_mov_b64_e32 v[92:93], v[4:5]
	v_mov_b64_e32 v[112:113], v[4:5]
	v_mov_b64_e32 v[104:105], v[4:5]
	v_mov_b64_e32 v[140:141], v[4:5]
	v_mov_b64_e32 v[108:109], v[4:5]
	v_mov_b64_e32 v[160:161], v[4:5]
	v_mov_b64_e32 v[152:153], v[4:5]
	v_mov_b64_e32 v[196:197], v[4:5]
	v_mov_b64_e32 v[156:157], v[4:5]
	s_mov_b32 s68, 0
	s_cselect_b64 s[22:23], -1, 0
	s_mov_b32 s69, 0x10e000
	s_movk_i32 s70, 0x80
	v_mov_b64_e32 v[14:15], v[2:3]
	v_mov_b64_e32 v[6:7], v[2:3]
	v_mov_b64_e32 v[18:19], v[2:3]
	v_mov_b64_e32 v[10:11], v[2:3]
	v_mov_b64_e32 v[30:31], v[2:3]
	v_mov_b64_e32 v[22:23], v[2:3]
	v_mov_b64_e32 v[34:35], v[2:3]
	v_mov_b64_e32 v[26:27], v[2:3]
	v_mov_b64_e32 v[46:47], v[2:3]
	v_mov_b64_e32 v[38:39], v[2:3]
	v_mov_b64_e32 v[50:51], v[2:3]
	v_mov_b64_e32 v[42:43], v[2:3]
	v_mov_b64_e32 v[62:63], v[2:3]
	v_mov_b64_e32 v[54:55], v[2:3]
	v_mov_b64_e32 v[66:67], v[2:3]
	v_mov_b64_e32 v[58:59], v[2:3]
	v_mov_b64_e32 v[78:79], v[2:3]
	v_mov_b64_e32 v[70:71], v[2:3]
	v_mov_b64_e32 v[82:83], v[2:3]
	v_mov_b64_e32 v[74:75], v[2:3]
	v_mov_b64_e32 v[94:95], v[2:3]
	v_mov_b64_e32 v[86:87], v[2:3]
	v_mov_b64_e32 v[98:99], v[2:3]
	v_mov_b64_e32 v[90:91], v[2:3]
	v_mov_b64_e32 v[110:111], v[2:3]
	v_mov_b64_e32 v[102:103], v[2:3]
	v_mov_b64_e32 v[138:139], v[2:3]
	v_mov_b64_e32 v[106:107], v[2:3]
	v_mov_b64_e32 v[158:159], v[2:3]
	v_mov_b64_e32 v[150:151], v[2:3]
	v_mov_b64_e32 v[194:195], v[2:3]
	v_mov_b64_e32 v[154:155], v[2:3]
	s_branch .LBB0_1175

; __device__ __forceinline__ float sigmoidf_(float x) { return __builtin_amdgcn_rcpf(1.0f + __builtin_amdgcn_exp2f(x * -1.4426950408889634f)); }
; __device__ __forceinline__ f32x4 rot1(const f32x4 a) { return (f32x4){a[1], a[2], a[3], a[0]}; }
; __device__ __forceinline__ u32x4 pack8(const f32x4 a, const f32x4 b) { u32x4 w; w.x = cvtpk(a[0], a[1]); w.y = cvtpk(a[2], a[3]); w.z = cvtpk(b[0], b[1]); w.w = cvtpk(b[2], b[3]); return w; }
; __device__ __forceinline__ void phase_moe_gu(const Ptrs& p, LAS unsigned char* lds) {
;     ...
;         const int c = n0 + T.wc * 32 + T.fq * 8;
;         const float* bg = p.b_gate + (size_t)mu.e * D + c; const float* bu = p.b_up + (size_t)mu.e * D + c;
;         const f32x4 bg0 = *(const f32x4*)bg, bg1 = *(const f32x4*)(bg + 4), bu0 = *(const f32x4*)bu, bu1 = *(const f32x4*)(bu + 4);
; #pragma unroll
;         for (int m = 0; m < 8; ++m) { const int r = i0 + T.wr * 128 + m * 16 + T.fr;
;             f32x4 g0 = acc[m][0] + bg0, g1 = rot1(acc[m][1]) + bg1, u0 = acc[m][2] + bu0, u1 = rot1(acc[m][3]) + bu1;
; #pragma unroll
;             for (int j = 0; j < 4; ++j) { float g = fminf(g0[j], 7.0f), uu = fminf(fmaxf(u0[j], -7.0f), 7.0f); g0[j] = (uu + 1.0f) * g * sigmoidf_(1.702f * g);
;                 g = fminf(g1[j], 7.0f); uu = fminf(fmaxf(u1[j], -7.0f), 7.0f); g1[j] = (uu + 1.0f) * g * sigmoidf_(1.702f * g); }
;             if (r < mu.cnt) __builtin_amdgcn_raw_buffer_store_b128(pack8(g0, g1), ract, (unsigned)(((mu.base + r) * D + c) * 2), 0, 16); }
.LBB0_1267:
	v_mov_b32_e32 v3, v0
	s_nop 0
	v_lshrrev_b32_e32 v4, 1, v3
	v_and_b32_e32 v4, 0x78, v4
	s_waitcnt vmcnt(3)
	v_or_b32_e32 v130, s0, v4
	s_lshl_b64 s[0:1], s[42:43], 13
	s_add_u32 s4, s50, s0
	v_ashrrev_i32_e32 v131, 31, v130
	s_addc_u32 s5, s51, s1
	v_lshlrev_b64 v[4:5], 2, v[130:131]
	v_lshl_add_u64 v[114:115], s[4:5], 0, v[4:5]
	v_readlane_b32 s4, v246, 0
	v_readlane_b32 s6, v246, 2
	v_readlane_b32 s7, v246, 3
	s_add_u32 s0, s6, s0
	s_addc_u32 s1, s7, s1
	v_lshl_add_u64 v[4:5], s[0:1], 0, v[4:5]
	global_load_dwordx4 v[126:129], v[114:115], off offset:16
	global_load_dwordx4 v[118:121], v[114:115], off
	s_nop 0
	global_load_dwordx4 v[114:117], v[4:5], off
	global_load_dwordx4 v[122:125], v[4:5], off offset:16
	v_ashrrev_i32_e32 v4, 1, v3
	v_and_b32_e32 v4, 0xffffff80, v4
	v_add_u32_e32 v4, s2, v4
	v_and_or_b32 v4, v3, 15, v4
	v_lshlrev_b32_e32 v3, 1, v130
	v_cmp_gt_i32_e32 vcc, s87, v4
	v_readlane_b32 s5, v246, 1
	v_readlane_b32 s8, v246, 4
	v_readlane_b32 s9, v246, 5
	v_readlane_b32 s10, v246, 6
	v_readlane_b32 s11, v246, 7
	s_waitcnt vmcnt(0)
	s_and_saveexec_b64 s[0:1], vcc
	s_cbranch_execz .LBB0_1269
	v_pk_mov_b32 v[130:131], v[194:195], v[196:197] op_sel:[1,0]
	v_add_f32_e32 v5, v159, v122
	v_pk_add_f32 v[130:131], v[130:131], v[126:127]
	v_med3_f32 v134, v5, s84, v214
	v_min_f32_e32 v130, 0x40e00000, v130
	v_min_f32_e32 v131, 0x40e00000, v131
	v_mul_f32_e32 v5, 0x3fd9db23, v130
	v_mul_f32_e32 v135, 0x3fd9db23, v131
	v_mul_f32_e32 v5, 0xbfb8aa3b, v5
	v_mul_f32_e32 v135, 0xbfb8aa3b, v135
	v_exp_f32_e32 v5, v5
	v_exp_f32_e32 v135, v135
	v_pk_mov_b32 v[132:133], v[196:197], v[194:195] op_sel:[1,0]
	s_mov_b32 s22, s26
	v_add_f32_e32 v5, 1.0, v5
	v_add_f32_e32 v135, 1.0, v135
	v_rcp_f32_e32 v136, v5
	v_add_f32_e32 v5, v160, v123
	v_rcp_f32_e32 v137, v135
	v_med3_f32 v135, v5, s84, v214
	v_pk_add_f32 v[134:135], v[134:135], 1.0 op_sel_hi:[1,0]
	v_pk_add_f32 v[132:133], v[132:133], v[128:129]
	v_pk_mul_f32 v[130:131], v[130:131], v[134:135]
	v_add_f32_e32 v5, v161, v124
	v_pk_mul_f32 v[134:135], v[130:131], v[136:137]
	v_min_f32_e32 v130, 0x40e00000, v132
	v_med3_f32 v132, v5, s84, v214
	v_mul_f32_e32 v5, 0x3fd9db23, v130
	v_min_f32_e32 v131, 0x40e00000, v133
	v_mul_f32_e32 v5, 0xbfb8aa3b, v5
	v_mul_f32_e32 v133, 0x3fd9db23, v131
	v_exp_f32_e32 v5, v5
	v_mul_f32_e32 v133, 0xbfb8aa3b, v133
	v_exp_f32_e32 v133, v133
	s_mov_b32 s23, s27
	v_add_f32_e32 v5, 1.0, v5
	v_rcp_f32_e32 v136, v5
	v_add_f32_e32 v5, v158, v125
	v_add_f32_e32 v133, 1.0, v133
	v_rcp_f32_e32 v137, v133
	v_med3_f32 v133, v5, s84, v214
	v_pk_add_f32 v[132:133], v[132:133], 1.0 op_sel_hi:[1,0]
	v_add_f32_e32 v5, v150, v114
	v_pk_mul_f32 v[130:131], v[130:131], v[132:133]
	v_pk_add_f32 v[132:133], v[154:155], v[118:119]
	v_med3_f32 v142, v5, s84, v214
	v_min_f32_e32 v132, 0x40e00000, v132
	v_mul_f32_e32 v5, 0x3fd9db23, v132
	v_min_f32_e32 v133, 0x40e00000, v133
	v_mul_f32_e32 v5, 0xbfb8aa3b, v5
	v_mul_f32_e32 v143, 0x3fd9db23, v133
	v_exp_f32_e32 v5, v5
	v_mul_f32_e32 v143, 0xbfb8aa3b, v143
	v_exp_f32_e32 v143, v143
	v_pk_mul_f32 v[136:137], v[130:131], v[136:137]
	v_add_f32_e32 v5, 1.0, v5
	v_rcp_f32_e32 v144, v5
	v_add_f32_e32 v5, v151, v115
	v_add_f32_e32 v143, 1.0, v143
	v_pk_add_f32 v[130:131], v[156:157], v[120:121]
	v_rcp_f32_e32 v145, v143
	v_med3_f32 v143, v5, s84, v214
	v_pk_add_f32 v[142:143], v[142:143], 1.0 op_sel_hi:[1,0]
	v_min_f32_e32 v130, 0x40e00000, v130
	v_add_f32_e32 v5, v152, v116
	v_min_f32_e32 v131, 0x40e00000, v131
	v_pk_mul_f32 v[132:133], v[132:133], v[142:143]
	v_med3_f32 v142, v5, s84, v214
	v_mul_f32_e32 v5, 0x3fd9db23, v130
	v_mul_f32_e32 v143, 0x3fd9db23, v131
	v_mul_f32_e32 v5, 0xbfb8aa3b, v5
	v_mul_f32_e32 v143, 0xbfb8aa3b, v143
	v_exp_f32_e32 v5, v5
	v_exp_f32_e32 v143, v143
	v_pk_mul_f32 v[132:133], v[132:133], v[144:145]
	v_add_f32_e32 v5, 1.0, v5
	v_add_f32_e32 v143, 1.0, v143
	v_rcp_f32_e32 v144, v5
	v_add_f32_e32 v5, v153, v117
	v_rcp_f32_e32 v145, v143
	v_med3_f32 v143, v5, s84, v214
	v_pk_add_f32 v[142:143], v[142:143], 1.0 op_sel_hi:[1,0]
	v_add_u32_e32 v5, s88, v4
	v_pk_mul_f32 v[130:131], v[130:131], v[142:143]
	v_lshl_add_u32 v5, v5, 12, v3
	v_pk_mul_f32 v[142:143], v[130:131], v[144:145]
	v_cvt_pk_bf16_f32 v130, v132, v133
	v_cvt_pk_bf16_f32 v131, v142, v143
	v_cvt_pk_bf16_f32 v132, v134, v135
	v_cvt_pk_bf16_f32 v133, v136, v137
	buffer_store_dwordx4 v[130:133], v5, s[20:23], 0 offen sc1
; __device__ __forceinline__ float sigmoidf_(float x) { return __builtin_amdgcn_rcpf(1.0f + __builtin_amdgcn_exp2f(x * -1.4426950408889634f)); }
; __device__ __forceinline__ f32x4 rot1(const f32x4 a) { return (f32x4){a[1], a[2], a[3], a[0]}; }
; __device__ __forceinline__ u32x4 pack8(const f32x4 a, const f32x4 b) { u32x4 w; w.x = cvtpk(a[0], a[1]); w.y = cvtpk(a[2], a[3]); w.z = cvtpk(b[0], b[1]); w.w = cvtpk(b[2], b[3]); return w; }
; __device__ __forceinline__ void phase_moe_gu(const Ptrs& p, LAS unsigned char* lds) {
;     ...
;         for (int m = 0; m < 8; ++m) { const int r = i0 + T.wr * 128 + m * 16 + T.fr;
;             f32x4 g0 = acc[m][0] + bg0, g1 = rot1(acc[m][1]) + bg1, u0 = acc[m][2] + bu0, u1 = rot1(acc[m][3]) + bu1;
; #pragma unroll
;             for (int j = 0; j < 4; ++j) { float g = fminf(g0[j], 7.0f), uu = fminf(fmaxf(u0[j], -7.0f), 7.0f); g0[j] = (uu + 1.0f) * g * sigmoidf_(1.702f * g);
;                 g = fminf(g1[j], 7.0f); uu = fminf(fmaxf(u1[j], -7.0f), 7.0f); g1[j] = (uu + 1.0f) * g * sigmoidf_(1.702f * g); }
;             if (r < mu.cnt) __builtin_amdgcn_raw_buffer_store_b128(pack8(g0, g1), ract, (unsigned)(((mu.base + r) * D + c) * 2), 0, 16); }
.LBB0_1269:
	s_or_b64 exec, exec, s[0:1]
	v_or_b32_e32 v5, 16, v4
	v_cmp_gt_i32_e32 vcc, s87, v5
	s_and_saveexec_b64 s[0:1], vcc
	s_cbranch_execz .LBB0_1271
	v_pk_mov_b32 v[130:131], v[138:139], v[140:141] op_sel:[1,0]
	v_add_f32_e32 v111, v111, v122
	v_pk_add_f32 v[130:131], v[130:131], v[126:127]
	v_med3_f32 v134, v111, s84, v214
	v_min_f32_e32 v130, 0x40e00000, v130
	v_mul_f32_e32 v111, 0x3fd9db23, v130
	v_min_f32_e32 v131, 0x40e00000, v131
	v_mul_f32_e32 v111, 0xbfb8aa3b, v111
	v_mul_f32_e32 v135, 0x3fd9db23, v131
	v_exp_f32_e32 v111, v111
	v_mul_f32_e32 v135, 0xbfb8aa3b, v135
	v_exp_f32_e32 v135, v135
	v_pk_mov_b32 v[132:133], v[140:141], v[138:139] op_sel:[1,0]
	v_add_f32_e32 v111, 1.0, v111
	v_pk_add_f32 v[132:133], v[132:133], v[128:129]
	v_rcp_f32_e32 v136, v111
	v_add_f32_e32 v111, v112, v123
	v_add_f32_e32 v112, 1.0, v135
	v_rcp_f32_e32 v137, v112
	v_med3_f32 v135, v111, s84, v214
	v_min_f32_e32 v112, 0x40e00000, v132
	v_add_f32_e32 v111, v113, v124
	v_med3_f32 v132, v111, s84, v214
	v_mul_f32_e32 v111, 0x3fd9db23, v112
	v_min_f32_e32 v113, 0x40e00000, v133
	v_mul_f32_e32 v111, 0xbfb8aa3b, v111
	v_mul_f32_e32 v133, 0x3fd9db23, v113
	v_exp_f32_e32 v111, v111
	v_mul_f32_e32 v133, 0xbfb8aa3b, v133
	v_exp_f32_e32 v133, v133
	v_pk_add_f32 v[134:135], v[134:135], 1.0 op_sel_hi:[1,0]
	v_add_f32_e32 v111, 1.0, v111
	v_add_f32_e32 v110, v110, v125
	v_add_f32_e32 v102, v102, v114
	v_add_f32_e32 v103, v103, v115
	v_pk_mul_f32 v[130:131], v[130:131], v[134:135]
	v_rcp_f32_e32 v134, v111
	v_add_f32_e32 v111, 1.0, v133
	v_med3_f32 v133, v110, s84, v214
	v_pk_add_f32 v[106:107], v[106:107], v[118:119]
	v_med3_f32 v102, v102, s84, v214
	v_med3_f32 v103, v103, s84, v214
	v_rcp_f32_e32 v135, v111
	v_pk_add_f32 v[110:111], v[132:133], 1.0 op_sel_hi:[1,0]
	v_pk_add_f32 v[108:109], v[108:109], v[120:121]
	v_min_f32_e32 v106, 0x40e00000, v106
	v_min_f32_e32 v107, 0x40e00000, v107
	v_pk_add_f32 v[102:103], v[102:103], 1.0 op_sel_hi:[1,0]
	v_pk_mul_f32 v[110:111], v[112:113], v[110:111]
	v_mul_f32_e32 v112, 0x3fd9db23, v106
	v_pk_mul_f32 v[102:103], v[106:107], v[102:103]
	v_min_f32_e32 v106, 0x40e00000, v108
	v_mul_f32_e32 v113, 0x3fd9db23, v107
	v_mul_f32_e32 v107, 0x3fd9db23, v106
	v_mul_f32_e32 v107, 0xbfb8aa3b, v107
	v_exp_f32_e32 v108, v107
	v_min_f32_e32 v107, 0x40e00000, v109
	v_mul_f32_e32 v109, 0x3fd9db23, v107
	v_mul_f32_e32 v112, 0xbfb8aa3b, v112
	v_mul_f32_e32 v113, 0xbfb8aa3b, v113
	v_mul_f32_e32 v109, 0xbfb8aa3b, v109
	v_exp_f32_e32 v112, v112
	v_exp_f32_e32 v113, v113
	v_exp_f32_e32 v109, v109
	v_add_f32_e32 v108, 1.0, v108
	v_add_f32_e32 v112, 1.0, v112
	v_add_f32_e32 v113, 1.0, v113
	v_add_f32_e32 v109, 1.0, v109
	v_rcp_f32_e32 v112, v112
	v_rcp_f32_e32 v113, v113
	v_add_f32_e32 v104, v104, v116
	v_rcp_f32_e32 v108, v108
	v_add_f32_e32 v105, v105, v117
	v_rcp_f32_e32 v109, v109
	v_med3_f32 v104, v104, s84, v214
	v_med3_f32 v105, v105, s84, v214
	v_pk_add_f32 v[104:105], v[104:105], 1.0 op_sel_hi:[1,0]
	v_pk_mul_f32 v[130:131], v[130:131], v[136:137]
	v_pk_mul_f32 v[104:105], v[106:107], v[104:105]
	v_pk_mul_f32 v[110:111], v[110:111], v[134:135]
	v_pk_mul_f32 v[102:103], v[102:103], v[112:113]
	v_pk_mul_f32 v[104:105], v[104:105], v[108:109]
	v_add_u32_e32 v5, s88, v5
	v_cvt_pk_bf16_f32 v102, v102, v103
	v_cvt_pk_bf16_f32 v103, v104, v105
	v_cvt_pk_bf16_f32 v104, v130, v131
	v_cvt_pk_bf16_f32 v105, v110, v111
	v_lshl_add_u32 v5, v5, 12, v3
	s_mov_b32 s22, s26
	s_mov_b32 s23, s27
	buffer_store_dwordx4 v[102:105], v5, s[20:23], 0 offen sc1
.LBB0_1271:
	s_or_b64 exec, exec, s[0:1]
	v_or_b32_e32 v5, 32, v4
	v_cmp_gt_i32_e32 vcc, s87, v5
	s_and_saveexec_b64 s[0:1], vcc
	s_cbranch_execz .LBB0_1273
	v_pk_mov_b32 v[102:103], v[98:99], v[100:101] op_sel:[1,0]
	v_pk_mov_b32 v[98:99], v[100:101], v[98:99] op_sel:[1,0]
	v_pk_add_f32 v[100:101], v[102:103], v[126:127]
	v_add_f32_e32 v95, v95, v122
	v_min_f32_e32 v100, 0x40e00000, v100
	v_med3_f32 v102, v95, s84, v214
	v_mul_f32_e32 v95, 0x3fd9db23, v100
	v_min_f32_e32 v101, 0x40e00000, v101
	v_mul_f32_e32 v95, 0xbfb8aa3b, v95
	v_mul_f32_e32 v103, 0x3fd9db23, v101
	v_exp_f32_e32 v95, v95
	v_mul_f32_e32 v103, 0xbfb8aa3b, v103
	v_exp_f32_e32 v103, v103
	v_pk_add_f32 v[98:99], v[98:99], v[128:129]
	v_add_f32_e32 v95, 1.0, v95
	v_rcp_f32_e32 v104, v95
	v_add_f32_e32 v95, v96, v123
	v_add_f32_e32 v96, 1.0, v103
	v_rcp_f32_e32 v105, v96
	v_med3_f32 v103, v95, s84, v214
	v_min_f32_e32 v96, 0x40e00000, v98
	v_add_f32_e32 v95, v97, v124
	v_med3_f32 v98, v95, s84, v214
	v_mul_f32_e32 v95, 0x3fd9db23, v96
	v_min_f32_e32 v97, 0x40e00000, v99
	v_mul_f32_e32 v95, 0xbfb8aa3b, v95
	v_mul_f32_e32 v99, 0x3fd9db23, v97
	v_exp_f32_e32 v95, v95
	v_mul_f32_e32 v99, 0xbfb8aa3b, v99
	v_exp_f32_e32 v99, v99
	v_pk_add_f32 v[102:103], v[102:103], 1.0 op_sel_hi:[1,0]
	v_add_f32_e32 v95, 1.0, v95
	v_add_f32_e32 v94, v94, v125
	v_add_f32_e32 v86, v86, v114
	v_add_f32_e32 v87, v87, v115
	v_pk_mul_f32 v[100:101], v[100:101], v[102:103]
	v_rcp_f32_e32 v102, v95
	v_add_f32_e32 v95, 1.0, v99
	v_med3_f32 v99, v94, s84, v214
	v_pk_add_f32 v[90:91], v[90:91], v[118:119]
	v_med3_f32 v86, v86, s84, v214
	v_med3_f32 v87, v87, s84, v214
	v_rcp_f32_e32 v103, v95
	v_pk_add_f32 v[94:95], v[98:99], 1.0 op_sel_hi:[1,0]
	v_pk_add_f32 v[92:93], v[92:93], v[120:121]
	v_min_f32_e32 v90, 0x40e00000, v90
	v_min_f32_e32 v91, 0x40e00000, v91
	v_pk_add_f32 v[86:87], v[86:87], 1.0 op_sel_hi:[1,0]
	v_pk_mul_f32 v[94:95], v[96:97], v[94:95]
	v_mul_f32_e32 v96, 0x3fd9db23, v90
	v_pk_mul_f32 v[86:87], v[90:91], v[86:87]
	v_min_f32_e32 v90, 0x40e00000, v92
	v_mul_f32_e32 v97, 0x3fd9db23, v91
	v_mul_f32_e32 v91, 0x3fd9db23, v90
	v_mul_f32_e32 v91, 0xbfb8aa3b, v91
	v_exp_f32_e32 v92, v91
	v_min_f32_e32 v91, 0x40e00000, v93
	v_mul_f32_e32 v93, 0x3fd9db23, v91
	v_mul_f32_e32 v96, 0xbfb8aa3b, v96
	v_mul_f32_e32 v97, 0xbfb8aa3b, v97
	v_mul_f32_e32 v93, 0xbfb8aa3b, v93
	v_exp_f32_e32 v96, v96
	v_exp_f32_e32 v97, v97
	v_exp_f32_e32 v93, v93
	v_add_f32_e32 v92, 1.0, v92
	v_add_f32_e32 v96, 1.0, v96
	v_add_f32_e32 v97, 1.0, v97
	v_add_f32_e32 v93, 1.0, v93
	v_rcp_f32_e32 v96, v96
	v_rcp_f32_e32 v97, v97
	v_add_f32_e32 v88, v88, v116
	v_rcp_f32_e32 v92, v92
	v_add_f32_e32 v89, v89, v117
	v_rcp_f32_e32 v93, v93
	v_med3_f32 v88, v88, s84, v214
	v_med3_f32 v89, v89, s84, v214
	v_pk_add_f32 v[88:89], v[88:89], 1.0 op_sel_hi:[1,0]
	v_pk_mul_f32 v[100:101], v[100:101], v[104:105]
	v_pk_mul_f32 v[88:89], v[90:91], v[88:89]
	v_pk_mul_f32 v[94:95], v[94:95], v[102:103]
	v_pk_mul_f32 v[86:87], v[86:87], v[96:97]
	v_pk_mul_f32 v[88:89], v[88:89], v[92:93]
	v_add_u32_e32 v5, s88, v5
	v_cvt_pk_bf16_f32 v86, v86, v87
	v_cvt_pk_bf16_f32 v87, v88, v89
	v_cvt_pk_bf16_f32 v88, v100, v101
	v_cvt_pk_bf16_f32 v89, v94, v95
	v_lshl_add_u32 v5, v5, 12, v3
	s_mov_b32 s22, s26
	s_mov_b32 s23, s27
	buffer_store_dwordx4 v[86:89], v5, s[20:23], 0 offen sc1
; __device__ __forceinline__ float sigmoidf_(float x) { return __builtin_amdgcn_rcpf(1.0f + __builtin_amdgcn_exp2f(x * -1.4426950408889634f)); }
; __device__ __forceinline__ f32x4 rot1(const f32x4 a) { return (f32x4){a[1], a[2], a[3], a[0]}; }
; __device__ __forceinline__ u32x4 pack8(const f32x4 a, const f32x4 b) { u32x4 w; w.x = cvtpk(a[0], a[1]); w.y = cvtpk(a[2], a[3]); w.z = cvtpk(b[0], b[1]); w.w = cvtpk(b[2], b[3]); return w; }
; __device__ __forceinline__ void phase_moe_gu(const Ptrs& p, LAS unsigned char* lds) {
;     ...
;         for (int m = 0; m < 8; ++m) { const int r = i0 + T.wr * 128 + m * 16 + T.fr;
;             f32x4 g0 = acc[m][0] + bg0, g1 = rot1(acc[m][1]) + bg1, u0 = acc[m][2] + bu0, u1 = rot1(acc[m][3]) + bu1;
; #pragma unroll
;             for (int j = 0; j < 4; ++j) { float g = fminf(g0[j], 7.0f), uu = fminf(fmaxf(u0[j], -7.0f), 7.0f); g0[j] = (uu + 1.0f) * g * sigmoidf_(1.702f * g);
;                 g = fminf(g1[j], 7.0f); uu = fminf(fmaxf(u1[j], -7.0f), 7.0f); g1[j] = (uu + 1.0f) * g * sigmoidf_(1.702f * g); }
;             if (r < mu.cnt) __builtin_amdgcn_raw_buffer_store_b128(pack8(g0, g1), ract, (unsigned)(((mu.base + r) * D + c) * 2), 0, 16); }
.LBB0_1273:
	s_or_b64 exec, exec, s[0:1]
	v_or_b32_e32 v5, 48, v4
	v_cmp_gt_i32_e32 vcc, s87, v5
	s_and_saveexec_b64 s[0:1], vcc
	s_cbranch_execz .LBB0_1275
	v_pk_mov_b32 v[86:87], v[82:83], v[84:85] op_sel:[1,0]
	v_pk_mov_b32 v[82:83], v[84:85], v[82:83] op_sel:[1,0]
	v_pk_add_f32 v[84:85], v[86:87], v[126:127]
	v_add_f32_e32 v79, v79, v122
	v_min_f32_e32 v84, 0x40e00000, v84
	v_med3_f32 v86, v79, s84, v214
	v_mul_f32_e32 v79, 0x3fd9db23, v84
	v_min_f32_e32 v85, 0x40e00000, v85
	v_mul_f32_e32 v79, 0xbfb8aa3b, v79
	v_mul_f32_e32 v87, 0x3fd9db23, v85
	v_exp_f32_e32 v79, v79
	v_mul_f32_e32 v87, 0xbfb8aa3b, v87
	v_exp_f32_e32 v87, v87
	v_pk_add_f32 v[82:83], v[82:83], v[128:129]
	v_add_f32_e32 v79, 1.0, v79
	v_rcp_f32_e32 v88, v79
	v_add_f32_e32 v79, v80, v123
	v_add_f32_e32 v80, 1.0, v87
	v_rcp_f32_e32 v89, v80
	v_med3_f32 v87, v79, s84, v214
	v_min_f32_e32 v80, 0x40e00000, v82
	v_add_f32_e32 v79, v81, v124
	v_med3_f32 v82, v79, s84, v214
	v_mul_f32_e32 v79, 0x3fd9db23, v80
	v_min_f32_e32 v81, 0x40e00000, v83
	v_mul_f32_e32 v79, 0xbfb8aa3b, v79
	v_mul_f32_e32 v83, 0x3fd9db23, v81
	v_exp_f32_e32 v79, v79
	v_mul_f32_e32 v83, 0xbfb8aa3b, v83
	v_exp_f32_e32 v83, v83
	v_pk_add_f32 v[86:87], v[86:87], 1.0 op_sel_hi:[1,0]
	v_add_f32_e32 v79, 1.0, v79
	v_add_f32_e32 v78, v78, v125
	v_add_f32_e32 v70, v70, v114
	v_add_f32_e32 v71, v71, v115
	v_pk_mul_f32 v[84:85], v[84:85], v[86:87]
	v_rcp_f32_e32 v86, v79
	v_add_f32_e32 v79, 1.0, v83
	v_med3_f32 v83, v78, s84, v214
	v_pk_add_f32 v[74:75], v[74:75], v[118:119]
	v_med3_f32 v70, v70, s84, v214
	v_med3_f32 v71, v71, s84, v214
	v_rcp_f32_e32 v87, v79
	v_pk_add_f32 v[78:79], v[82:83], 1.0 op_sel_hi:[1,0]
	v_pk_add_f32 v[76:77], v[76:77], v[120:121]
	v_min_f32_e32 v74, 0x40e00000, v74
	v_min_f32_e32 v75, 0x40e00000, v75
	v_pk_add_f32 v[70:71], v[70:71], 1.0 op_sel_hi:[1,0]
	v_pk_mul_f32 v[78:79], v[80:81], v[78:79]
	v_mul_f32_e32 v80, 0x3fd9db23, v74
	v_pk_mul_f32 v[70:71], v[74:75], v[70:71]
	v_min_f32_e32 v74, 0x40e00000, v76
	v_mul_f32_e32 v81, 0x3fd9db23, v75
	v_mul_f32_e32 v75, 0x3fd9db23, v74
	v_mul_f32_e32 v75, 0xbfb8aa3b, v75
	v_exp_f32_e32 v76, v75
	v_min_f32_e32 v75, 0x40e00000, v77
	v_mul_f32_e32 v77, 0x3fd9db23, v75
	v_mul_f32_e32 v80, 0xbfb8aa3b, v80
	v_mul_f32_e32 v81, 0xbfb8aa3b, v81
	v_mul_f32_e32 v77, 0xbfb8aa3b, v77
	v_exp_f32_e32 v80, v80
	v_exp_f32_e32 v81, v81
	v_exp_f32_e32 v77, v77
	v_add_f32_e32 v76, 1.0, v76
	v_add_f32_e32 v80, 1.0, v80
	v_add_f32_e32 v81, 1.0, v81
	v_add_f32_e32 v77, 1.0, v77
	v_rcp_f32_e32 v80, v80
	v_rcp_f32_e32 v81, v81
	v_add_f32_e32 v72, v72, v116
	v_rcp_f32_e32 v76, v76
	v_add_f32_e32 v73, v73, v117
	v_rcp_f32_e32 v77, v77
	v_med3_f32 v72, v72, s84, v214
	v_med3_f32 v73, v73, s84, v214
	v_pk_add_f32 v[72:73], v[72:73], 1.0 op_sel_hi:[1,0]
	v_pk_mul_f32 v[84:85], v[84:85], v[88:89]
	v_pk_mul_f32 v[72:73], v[74:75], v[72:73]
	v_pk_mul_f32 v[78:79], v[78:79], v[86:87]
	v_pk_mul_f32 v[70:71], v[70:71], v[80:81]
	v_pk_mul_f32 v[72:73], v[72:73], v[76:77]
	v_add_u32_e32 v5, s88, v5
	v_cvt_pk_bf16_f32 v70, v70, v71
	v_cvt_pk_bf16_f32 v71, v72, v73
	v_cvt_pk_bf16_f32 v72, v84, v85
	v_cvt_pk_bf16_f32 v73, v78, v79
	v_lshl_add_u32 v5, v5, 12, v3
	s_mov_b32 s22, s26
	s_mov_b32 s23, s27
	buffer_store_dwordx4 v[70:73], v5, s[20:23], 0 offen sc1
.LBB0_1275:
	s_or_b64 exec, exec, s[0:1]
	v_or_b32_e32 v5, 64, v4
	v_cmp_gt_i32_e32 vcc, s87, v5
	s_and_saveexec_b64 s[0:1], vcc
	s_cbranch_execz .LBB0_1277
	v_pk_mov_b32 v[70:71], v[66:67], v[68:69] op_sel:[1,0]
	v_pk_mov_b32 v[66:67], v[68:69], v[66:67] op_sel:[1,0]
	v_pk_add_f32 v[68:69], v[70:71], v[126:127]
	v_add_f32_e32 v63, v63, v122
	v_min_f32_e32 v68, 0x40e00000, v68
	v_med3_f32 v70, v63, s84, v214
	v_mul_f32_e32 v63, 0x3fd9db23, v68
	v_min_f32_e32 v69, 0x40e00000, v69
	v_mul_f32_e32 v63, 0xbfb8aa3b, v63
	v_mul_f32_e32 v71, 0x3fd9db23, v69
	v_exp_f32_e32 v63, v63
	v_mul_f32_e32 v71, 0xbfb8aa3b, v71
	v_exp_f32_e32 v71, v71
	v_pk_add_f32 v[66:67], v[66:67], v[128:129]
	v_add_f32_e32 v63, 1.0, v63
	v_rcp_f32_e32 v72, v63
	v_add_f32_e32 v63, v64, v123
	v_add_f32_e32 v64, 1.0, v71
	v_rcp_f32_e32 v73, v64
	v_med3_f32 v71, v63, s84, v214
	v_min_f32_e32 v64, 0x40e00000, v66
	v_add_f32_e32 v63, v65, v124
	v_med3_f32 v66, v63, s84, v214
	v_mul_f32_e32 v63, 0x3fd9db23, v64
	v_min_f32_e32 v65, 0x40e00000, v67
	v_mul_f32_e32 v63, 0xbfb8aa3b, v63
	v_mul_f32_e32 v67, 0x3fd9db23, v65
	v_exp_f32_e32 v63, v63
	v_mul_f32_e32 v67, 0xbfb8aa3b, v67
	v_exp_f32_e32 v67, v67
	v_pk_add_f32 v[70:71], v[70:71], 1.0 op_sel_hi:[1,0]
	v_add_f32_e32 v63, 1.0, v63
	v_add_f32_e32 v62, v62, v125
	v_add_f32_e32 v54, v54, v114
	v_add_f32_e32 v55, v55, v115
	v_pk_mul_f32 v[68:69], v[68:69], v[70:71]
	v_rcp_f32_e32 v70, v63
	v_add_f32_e32 v63, 1.0, v67
	v_med3_f32 v67, v62, s84, v214
	v_pk_add_f32 v[58:59], v[58:59], v[118:119]
	v_med3_f32 v54, v54, s84, v214
	v_med3_f32 v55, v55, s84, v214
	v_rcp_f32_e32 v71, v63
	v_pk_add_f32 v[62:63], v[66:67], 1.0 op_sel_hi:[1,0]
	v_pk_add_f32 v[60:61], v[60:61], v[120:121]
	v_min_f32_e32 v58, 0x40e00000, v58
	v_min_f32_e32 v59, 0x40e00000, v59
	v_pk_add_f32 v[54:55], v[54:55], 1.0 op_sel_hi:[1,0]
	v_pk_mul_f32 v[62:63], v[64:65], v[62:63]
	v_mul_f32_e32 v64, 0x3fd9db23, v58
	v_pk_mul_f32 v[54:55], v[58:59], v[54:55]
	v_min_f32_e32 v58, 0x40e00000, v60
	v_mul_f32_e32 v65, 0x3fd9db23, v59
	v_mul_f32_e32 v59, 0x3fd9db23, v58
	v_mul_f32_e32 v59, 0xbfb8aa3b, v59
	v_exp_f32_e32 v60, v59
	v_min_f32_e32 v59, 0x40e00000, v61
	v_mul_f32_e32 v61, 0x3fd9db23, v59
	v_mul_f32_e32 v64, 0xbfb8aa3b, v64
	v_mul_f32_e32 v65, 0xbfb8aa3b, v65
	v_mul_f32_e32 v61, 0xbfb8aa3b, v61
	v_exp_f32_e32 v64, v64
	v_exp_f32_e32 v65, v65
	v_exp_f32_e32 v61, v61
	v_add_f32_e32 v60, 1.0, v60
	v_add_f32_e32 v64, 1.0, v64
	v_add_f32_e32 v65, 1.0, v65
	v_add_f32_e32 v61, 1.0, v61
	v_rcp_f32_e32 v64, v64
	v_rcp_f32_e32 v65, v65
	v_add_f32_e32 v56, v56, v116
	v_rcp_f32_e32 v60, v60
	v_add_f32_e32 v57, v57, v117
	v_rcp_f32_e32 v61, v61
	v_med3_f32 v56, v56, s84, v214
	v_med3_f32 v57, v57, s84, v214
	v_pk_add_f32 v[56:57], v[56:57], 1.0 op_sel_hi:[1,0]
	v_pk_mul_f32 v[68:69], v[68:69], v[72:73]
	v_pk_mul_f32 v[56:57], v[58:59], v[56:57]
	v_pk_mul_f32 v[62:63], v[62:63], v[70:71]
	v_pk_mul_f32 v[54:55], v[54:55], v[64:65]
	v_pk_mul_f32 v[56:57], v[56:57], v[60:61]
	v_add_u32_e32 v5, s88, v5
	v_cvt_pk_bf16_f32 v54, v54, v55
	v_cvt_pk_bf16_f32 v55, v56, v57
	v_cvt_pk_bf16_f32 v56, v68, v69
	v_cvt_pk_bf16_f32 v57, v62, v63
	v_lshl_add_u32 v5, v5, 12, v3
	s_mov_b32 s22, s26
	s_mov_b32 s23, s27
	buffer_store_dwordx4 v[54:57], v5, s[20:23], 0 offen sc1
; __device__ __forceinline__ float sigmoidf_(float x) { return __builtin_amdgcn_rcpf(1.0f + __builtin_amdgcn_exp2f(x * -1.4426950408889634f)); }
; __device__ __forceinline__ f32x4 rot1(const f32x4 a) { return (f32x4){a[1], a[2], a[3], a[0]}; }
; __device__ __forceinline__ u32x4 pack8(const f32x4 a, const f32x4 b) { u32x4 w; w.x = cvtpk(a[0], a[1]); w.y = cvtpk(a[2], a[3]); w.z = cvtpk(b[0], b[1]); w.w = cvtpk(b[2], b[3]); return w; }
; __device__ __forceinline__ void phase_moe_gu(const Ptrs& p, LAS unsigned char* lds) {
;     ...
;         for (int m = 0; m < 8; ++m) { const int r = i0 + T.wr * 128 + m * 16 + T.fr;
;             f32x4 g0 = acc[m][0] + bg0, g1 = rot1(acc[m][1]) + bg1, u0 = acc[m][2] + bu0, u1 = rot1(acc[m][3]) + bu1;
; #pragma unroll
;             for (int j = 0; j < 4; ++j) { float g = fminf(g0[j], 7.0f), uu = fminf(fmaxf(u0[j], -7.0f), 7.0f); g0[j] = (uu + 1.0f) * g * sigmoidf_(1.702f * g);
;                 g = fminf(g1[j], 7.0f); uu = fminf(fmaxf(u1[j], -7.0f), 7.0f); g1[j] = (uu + 1.0f) * g * sigmoidf_(1.702f * g); }
;             if (r < mu.cnt) __builtin_amdgcn_raw_buffer_store_b128(pack8(g0, g1), ract, (unsigned)(((mu.base + r) * D + c) * 2), 0, 16); }
.LBB0_1277:
	s_or_b64 exec, exec, s[0:1]
	v_or_b32_e32 v5, 0x50, v4
	v_cmp_gt_i32_e32 vcc, s87, v5
	s_and_saveexec_b64 s[0:1], vcc
	s_cbranch_execz .LBB0_1279
	v_pk_mov_b32 v[54:55], v[50:51], v[52:53] op_sel:[1,0]
	v_pk_mov_b32 v[50:51], v[52:53], v[50:51] op_sel:[1,0]
	v_pk_add_f32 v[52:53], v[54:55], v[126:127]
	v_add_f32_e32 v47, v47, v122
	v_min_f32_e32 v52, 0x40e00000, v52
	v_med3_f32 v54, v47, s84, v214
	v_mul_f32_e32 v47, 0x3fd9db23, v52
	v_min_f32_e32 v53, 0x40e00000, v53
	v_mul_f32_e32 v47, 0xbfb8aa3b, v47
	v_mul_f32_e32 v55, 0x3fd9db23, v53
	v_exp_f32_e32 v47, v47
	v_mul_f32_e32 v55, 0xbfb8aa3b, v55
	v_exp_f32_e32 v55, v55
	v_pk_add_f32 v[50:51], v[50:51], v[128:129]
	v_add_f32_e32 v47, 1.0, v47
	v_rcp_f32_e32 v56, v47
	v_add_f32_e32 v47, v48, v123
	v_add_f32_e32 v48, 1.0, v55
	v_rcp_f32_e32 v57, v48
	v_med3_f32 v55, v47, s84, v214
	v_min_f32_e32 v48, 0x40e00000, v50
	v_add_f32_e32 v47, v49, v124
	v_med3_f32 v50, v47, s84, v214
	v_mul_f32_e32 v47, 0x3fd9db23, v48
	v_min_f32_e32 v49, 0x40e00000, v51
	v_mul_f32_e32 v47, 0xbfb8aa3b, v47
	v_mul_f32_e32 v51, 0x3fd9db23, v49
	v_exp_f32_e32 v47, v47
	v_mul_f32_e32 v51, 0xbfb8aa3b, v51
	v_exp_f32_e32 v51, v51
	v_pk_add_f32 v[54:55], v[54:55], 1.0 op_sel_hi:[1,0]
	v_add_f32_e32 v47, 1.0, v47
	v_add_f32_e32 v46, v46, v125
	v_add_f32_e32 v38, v38, v114
	v_add_f32_e32 v39, v39, v115
	v_pk_mul_f32 v[52:53], v[52:53], v[54:55]
	v_rcp_f32_e32 v54, v47
	v_add_f32_e32 v47, 1.0, v51
	v_med3_f32 v51, v46, s84, v214
	v_pk_add_f32 v[42:43], v[42:43], v[118:119]
	v_med3_f32 v38, v38, s84, v214
	v_med3_f32 v39, v39, s84, v214
	v_rcp_f32_e32 v55, v47
	v_pk_add_f32 v[46:47], v[50:51], 1.0 op_sel_hi:[1,0]
	v_pk_add_f32 v[44:45], v[44:45], v[120:121]
	v_min_f32_e32 v42, 0x40e00000, v42
	v_min_f32_e32 v43, 0x40e00000, v43
	v_pk_add_f32 v[38:39], v[38:39], 1.0 op_sel_hi:[1,0]
	v_pk_mul_f32 v[46:47], v[48:49], v[46:47]
	v_mul_f32_e32 v48, 0x3fd9db23, v42
	v_pk_mul_f32 v[38:39], v[42:43], v[38:39]
	v_min_f32_e32 v42, 0x40e00000, v44
	v_mul_f32_e32 v49, 0x3fd9db23, v43
	v_mul_f32_e32 v43, 0x3fd9db23, v42
	v_mul_f32_e32 v43, 0xbfb8aa3b, v43
	v_exp_f32_e32 v44, v43
	v_min_f32_e32 v43, 0x40e00000, v45
	v_mul_f32_e32 v45, 0x3fd9db23, v43
	v_mul_f32_e32 v48, 0xbfb8aa3b, v48
	v_mul_f32_e32 v49, 0xbfb8aa3b, v49
	v_mul_f32_e32 v45, 0xbfb8aa3b, v45
	v_exp_f32_e32 v48, v48
	v_exp_f32_e32 v49, v49
	v_exp_f32_e32 v45, v45
	v_add_f32_e32 v44, 1.0, v44
	v_add_f32_e32 v48, 1.0, v48
	v_add_f32_e32 v49, 1.0, v49
	v_add_f32_e32 v45, 1.0, v45
	v_rcp_f32_e32 v48, v48
	v_rcp_f32_e32 v49, v49
	v_add_f32_e32 v40, v40, v116
	v_rcp_f32_e32 v44, v44
	v_add_f32_e32 v41, v41, v117
	v_rcp_f32_e32 v45, v45
	v_med3_f32 v40, v40, s84, v214
	v_med3_f32 v41, v41, s84, v214
	v_pk_add_f32 v[40:41], v[40:41], 1.0 op_sel_hi:[1,0]
	v_pk_mul_f32 v[52:53], v[52:53], v[56:57]
	v_pk_mul_f32 v[40:41], v[42:43], v[40:41]
	v_pk_mul_f32 v[46:47], v[46:47], v[54:55]
	v_pk_mul_f32 v[38:39], v[38:39], v[48:49]
	v_pk_mul_f32 v[40:41], v[40:41], v[44:45]
	v_add_u32_e32 v5, s88, v5
	v_cvt_pk_bf16_f32 v38, v38, v39
	v_cvt_pk_bf16_f32 v39, v40, v41
	v_cvt_pk_bf16_f32 v40, v52, v53
	v_cvt_pk_bf16_f32 v41, v46, v47
	v_lshl_add_u32 v5, v5, 12, v3
	s_mov_b32 s22, s26
	s_mov_b32 s23, s27
	buffer_store_dwordx4 v[38:41], v5, s[20:23], 0 offen sc1
; __device__ __forceinline__ float sigmoidf_(float x) { return __builtin_amdgcn_rcpf(1.0f + __builtin_amdgcn_exp2f(x * -1.4426950408889634f)); }
; __device__ __forceinline__ f32x4 rot1(const f32x4 a) { return (f32x4){a[1], a[2], a[3], a[0]}; }
; __device__ __forceinline__ u32x4 pack8(const f32x4 a, const f32x4 b) { u32x4 w; w.x = cvtpk(a[0], a[1]); w.y = cvtpk(a[2], a[3]); w.z = cvtpk(b[0], b[1]); w.w = cvtpk(b[2], b[3]); return w; }
; __device__ __forceinline__ void phase_moe_gu(const Ptrs& p, LAS unsigned char* lds) {
;     ...
;         for (int m = 0; m < 8; ++m) { const int r = i0 + T.wr * 128 + m * 16 + T.fr;
;             f32x4 g0 = acc[m][0] + bg0, g1 = rot1(acc[m][1]) + bg1, u0 = acc[m][2] + bu0, u1 = rot1(acc[m][3]) + bu1;
; #pragma unroll
;             for (int j = 0; j < 4; ++j) { float g = fminf(g0[j], 7.0f), uu = fminf(fmaxf(u0[j], -7.0f), 7.0f); g0[j] = (uu + 1.0f) * g * sigmoidf_(1.702f * g);
;                 g = fminf(g1[j], 7.0f); uu = fminf(fmaxf(u1[j], -7.0f), 7.0f); g1[j] = (uu + 1.0f) * g * sigmoidf_(1.702f * g); }
;             if (r < mu.cnt) __builtin_amdgcn_raw_buffer_store_b128(pack8(g0, g1), ract, (unsigned)(((mu.base + r) * D + c) * 2), 0, 16); }
.LBB0_1279:
	s_or_b64 exec, exec, s[0:1]
	v_or_b32_e32 v5, 0x60, v4
	v_cmp_gt_i32_e32 vcc, s87, v5
	s_and_saveexec_b64 s[0:1], vcc
	s_cbranch_execz .LBB0_1281
	v_pk_mov_b32 v[38:39], v[34:35], v[36:37] op_sel:[1,0]
	v_pk_mov_b32 v[34:35], v[36:37], v[34:35] op_sel:[1,0]
	v_pk_add_f32 v[36:37], v[38:39], v[126:127]
	v_add_f32_e32 v31, v31, v122
	v_min_f32_e32 v36, 0x40e00000, v36
	v_med3_f32 v38, v31, s84, v214
	v_mul_f32_e32 v31, 0x3fd9db23, v36
	v_min_f32_e32 v37, 0x40e00000, v37
	v_mul_f32_e32 v31, 0xbfb8aa3b, v31
	v_mul_f32_e32 v39, 0x3fd9db23, v37
	v_exp_f32_e32 v31, v31
	v_mul_f32_e32 v39, 0xbfb8aa3b, v39
	v_exp_f32_e32 v39, v39
	v_pk_add_f32 v[34:35], v[34:35], v[128:129]
	v_add_f32_e32 v31, 1.0, v31
	v_rcp_f32_e32 v40, v31
	v_add_f32_e32 v31, v32, v123
	v_add_f32_e32 v32, 1.0, v39
	v_rcp_f32_e32 v41, v32
	v_med3_f32 v39, v31, s84, v214
	v_min_f32_e32 v32, 0x40e00000, v34
	v_add_f32_e32 v31, v33, v124
	v_med3_f32 v34, v31, s84, v214
	v_mul_f32_e32 v31, 0x3fd9db23, v32
	v_min_f32_e32 v33, 0x40e00000, v35
	v_mul_f32_e32 v31, 0xbfb8aa3b, v31
	v_mul_f32_e32 v35, 0x3fd9db23, v33
	v_exp_f32_e32 v31, v31
	v_mul_f32_e32 v35, 0xbfb8aa3b, v35
	v_exp_f32_e32 v35, v35
	v_pk_add_f32 v[38:39], v[38:39], 1.0 op_sel_hi:[1,0]
	v_add_f32_e32 v31, 1.0, v31
	v_add_f32_e32 v30, v30, v125
	v_add_f32_e32 v22, v22, v114
	v_add_f32_e32 v23, v23, v115
	v_pk_mul_f32 v[36:37], v[36:37], v[38:39]
	v_rcp_f32_e32 v38, v31
	v_add_f32_e32 v31, 1.0, v35
	v_med3_f32 v35, v30, s84, v214
	v_pk_add_f32 v[26:27], v[26:27], v[118:119]
	v_med3_f32 v22, v22, s84, v214
	v_med3_f32 v23, v23, s84, v214
	v_rcp_f32_e32 v39, v31
	v_pk_add_f32 v[30:31], v[34:35], 1.0 op_sel_hi:[1,0]
	v_pk_add_f32 v[28:29], v[28:29], v[120:121]
	v_min_f32_e32 v26, 0x40e00000, v26
	v_min_f32_e32 v27, 0x40e00000, v27
	v_pk_add_f32 v[22:23], v[22:23], 1.0 op_sel_hi:[1,0]
	v_pk_mul_f32 v[30:31], v[32:33], v[30:31]
	v_mul_f32_e32 v32, 0x3fd9db23, v26
	v_pk_mul_f32 v[22:23], v[26:27], v[22:23]
	v_min_f32_e32 v26, 0x40e00000, v28
	v_mul_f32_e32 v33, 0x3fd9db23, v27
	v_mul_f32_e32 v27, 0x3fd9db23, v26
	v_mul_f32_e32 v27, 0xbfb8aa3b, v27
	v_exp_f32_e32 v28, v27
	v_min_f32_e32 v27, 0x40e00000, v29
	v_mul_f32_e32 v29, 0x3fd9db23, v27
	v_mul_f32_e32 v32, 0xbfb8aa3b, v32
	v_mul_f32_e32 v33, 0xbfb8aa3b, v33
	v_mul_f32_e32 v29, 0xbfb8aa3b, v29
	v_exp_f32_e32 v32, v32
	v_exp_f32_e32 v33, v33
	v_exp_f32_e32 v29, v29
	v_add_f32_e32 v28, 1.0, v28
	v_add_f32_e32 v32, 1.0, v32
	v_add_f32_e32 v33, 1.0, v33
	v_add_f32_e32 v29, 1.0, v29
	v_rcp_f32_e32 v32, v32
	v_rcp_f32_e32 v33, v33
	v_add_f32_e32 v24, v24, v116
	v_rcp_f32_e32 v28, v28
	v_add_f32_e32 v25, v25, v117
	v_rcp_f32_e32 v29, v29
	v_med3_f32 v24, v24, s84, v214
	v_med3_f32 v25, v25, s84, v214
	v_pk_add_f32 v[24:25], v[24:25], 1.0 op_sel_hi:[1,0]
	v_pk_mul_f32 v[36:37], v[36:37], v[40:41]
	v_pk_mul_f32 v[24:25], v[26:27], v[24:25]
	v_pk_mul_f32 v[30:31], v[30:31], v[38:39]
	v_pk_mul_f32 v[22:23], v[22:23], v[32:33]
	v_pk_mul_f32 v[24:25], v[24:25], v[28:29]
	v_add_u32_e32 v5, s88, v5
	v_cvt_pk_bf16_f32 v22, v22, v23
	v_cvt_pk_bf16_f32 v23, v24, v25
	v_cvt_pk_bf16_f32 v24, v36, v37
	v_cvt_pk_bf16_f32 v25, v30, v31
	v_lshl_add_u32 v5, v5, 12, v3
	s_mov_b32 s22, s26
	s_mov_b32 s23, s27
	buffer_store_dwordx4 v[22:25], v5, s[20:23], 0 offen sc1
.LBB0_1281:
	s_or_b64 exec, exec, s[0:1]
	v_or_b32_e32 v4, 0x70, v4
	v_cmp_gt_i32_e32 vcc, s87, v4
	s_and_saveexec_b64 s[0:1], vcc
	s_cbranch_execz .LBB0_1283
	v_pk_mov_b32 v[22:23], v[18:19], v[20:21] op_sel:[1,0]
	v_pk_mov_b32 v[18:19], v[20:21], v[18:19] op_sel:[1,0]
	v_pk_add_f32 v[20:21], v[22:23], v[126:127]
	v_add_f32_e32 v5, v15, v122
	v_min_f32_e32 v20, 0x40e00000, v20
	v_med3_f32 v22, v5, s84, v214
	v_mul_f32_e32 v5, 0x3fd9db23, v20
	v_mul_f32_e32 v5, 0xbfb8aa3b, v5
	v_exp_f32_e32 v5, v5
	v_min_f32_e32 v21, 0x40e00000, v21
	v_mul_f32_e32 v15, 0x3fd9db23, v21
	v_mul_f32_e32 v15, 0xbfb8aa3b, v15
	v_exp_f32_e32 v15, v15
	v_add_f32_e32 v5, 1.0, v5
	v_pk_add_f32 v[18:19], v[18:19], v[128:129]
	v_rcp_f32_e32 v24, v5
	v_add_f32_e32 v5, v16, v123
	v_med3_f32 v23, v5, s84, v214
	v_min_f32_e32 v16, 0x40e00000, v18
	v_add_f32_e32 v5, v17, v124
	v_med3_f32 v18, v5, s84, v214
	v_mul_f32_e32 v5, 0x3fd9db23, v16
	v_add_f32_e32 v15, 1.0, v15
	v_mul_f32_e32 v5, 0xbfb8aa3b, v5
	v_min_f32_e32 v17, 0x40e00000, v19
	v_rcp_f32_e32 v25, v15
	v_exp_f32_e32 v5, v5
	v_mul_f32_e32 v15, 0x3fd9db23, v17
	v_mul_f32_e32 v15, 0xbfb8aa3b, v15
	v_exp_f32_e32 v15, v15
	v_pk_add_f32 v[22:23], v[22:23], 1.0 op_sel_hi:[1,0]
	v_add_f32_e32 v5, 1.0, v5
	v_pk_mul_f32 v[20:21], v[20:21], v[22:23]
	v_rcp_f32_e32 v22, v5
	v_add_f32_e32 v5, v14, v125
	v_pk_add_f32 v[10:11], v[10:11], v[118:119]
	v_add_f32_e32 v14, 1.0, v15
	v_med3_f32 v19, v5, s84, v214
	v_min_f32_e32 v10, 0x40e00000, v10
	v_add_f32_e32 v5, v6, v114
	v_rcp_f32_e32 v23, v14
	v_pk_add_f32 v[14:15], v[18:19], 1.0 op_sel_hi:[1,0]
	v_med3_f32 v6, v5, s84, v214
	v_mul_f32_e32 v5, 0x3fd9db23, v10
	v_min_f32_e32 v11, 0x40e00000, v11
	v_pk_mul_f32 v[14:15], v[16:17], v[14:15]
	v_mul_f32_e32 v5, 0xbfb8aa3b, v5
	v_mul_f32_e32 v16, 0x3fd9db23, v11
	v_exp_f32_e32 v5, v5
	v_mul_f32_e32 v16, 0xbfb8aa3b, v16
	v_exp_f32_e32 v17, v16
	v_pk_add_f32 v[12:13], v[12:13], v[120:121]
	v_add_f32_e32 v5, 1.0, v5
	v_rcp_f32_e32 v16, v5
	v_add_f32_e32 v5, v7, v115
	v_add_f32_e32 v7, 1.0, v17
	v_rcp_f32_e32 v17, v7
	v_med3_f32 v7, v5, s84, v214
	v_pk_add_f32 v[6:7], v[6:7], 1.0 op_sel_hi:[1,0]
	v_add_f32_e32 v5, v8, v116
	v_pk_mul_f32 v[6:7], v[10:11], v[6:7]
	v_min_f32_e32 v10, 0x40e00000, v12
	v_med3_f32 v8, v5, s84, v214
	v_mul_f32_e32 v5, 0x3fd9db23, v10
	v_min_f32_e32 v11, 0x40e00000, v13
	v_mul_f32_e32 v5, 0xbfb8aa3b, v5
	v_mul_f32_e32 v12, 0x3fd9db23, v11
	v_exp_f32_e32 v5, v5
	v_mul_f32_e32 v12, 0xbfb8aa3b, v12
	v_exp_f32_e32 v13, v12
	v_pk_mul_f32 v[20:21], v[20:21], v[24:25]
	v_add_f32_e32 v5, 1.0, v5
	v_rcp_f32_e32 v12, v5
	v_add_f32_e32 v5, v9, v117
	v_add_f32_e32 v9, 1.0, v13
	v_rcp_f32_e32 v13, v9
	v_med3_f32 v9, v5, s84, v214
	v_pk_add_f32 v[8:9], v[8:9], 1.0 op_sel_hi:[1,0]
	v_pk_mul_f32 v[14:15], v[14:15], v[22:23]
	v_pk_mul_f32 v[8:9], v[10:11], v[8:9]
	v_pk_mul_f32 v[6:7], v[6:7], v[16:17]
	v_pk_mul_f32 v[8:9], v[8:9], v[12:13]
	v_add_u32_e32 v4, s88, v4
	v_cvt_pk_bf16_f32 v6, v6, v7
	v_cvt_pk_bf16_f32 v7, v8, v9
	v_cvt_pk_bf16_f32 v8, v20, v21
	v_cvt_pk_bf16_f32 v9, v14, v15
	v_lshl_add_u32 v3, v4, 12, v3
	s_mov_b32 s22, s26
	s_mov_b32 s23, s27
	buffer_store_dwordx4 v[6:9], v3, s[20:23], 0 offen sc1

; #define LAS __attribute__((address_space(3)))
; __device__ __forceinline__ int tid_opaque() { int t = threadIdx.x; asm volatile("" : "+v"(t)); return t; }
;     __device__ __forceinline__ void init_epi() { const int tid = tid_opaque(), wid = tid >> 6, lane = tid & 63; wr = wid >> 2; wc = wid & 3; fr = lane & 15; fq = lane >> 4; }
; __device__ __forceinline__ f32x4 rot1(const f32x4 a) { return (f32x4){a[1], a[2], a[3], a[0]}; }
; __device__ __forceinline__ u32x4 pack8(const f32x4 a, const f32x4 b) { u32x4 w; w.x = cvtpk(a[0], a[1]); w.y = cvtpk(a[2], a[3]); w.z = cvtpk(b[0], b[1]); w.w = cvtpk(b[2], b[3]); return w; }
; __device__ __forceinline__ void phase_moe_down(const Ptrs& p, LAS unsigned char* lds) {
;     ...
; T.init_epi();
;         LAS int* tab = (LAS int*)(lds + GEMM_LDS);
;         { const int t_ = tid_opaque(); if (t_ < 256) { tab[2 * t_] = pa; tab[2 * t_ + 1] = __float_as_int(pg); } }
;         __syncthreads();
;         const float* bd = p.b_down + (size_t)mu.e * D;
; #pragma unroll
;         for (int m = 0; m < 8; ++m) { const int rl = T.wr * 128 + m * 16 + T.fr, r = i0 + rl;
;             if (r < mu.cnt) { const int a = tab[2 * rl]; const float gt = __int_as_float(tab[2 * rl + 1]);
; #pragma unroll
;                 for (int pp = 0; pp < 2; ++pp) { const int c = col0 + T.wc * 64 + pp * 32 + T.fq * 8;
;                     const f32x4 v0 = (acc[m][2 * pp] + *(const f32x4*)(bd + c)) * gt, v1 = (rot1(acc[m][2 * pp + 1]) + *(const f32x4*)(bd + c + 4)) * gt;
;                     *(u32x4*)(y + (size_t)a * D + c) = pack8(v0, v1); } } }
.LBB0_1580:
	s_or_b64 exec, exec, s[4:5]
	v_readlane_b32 s4, v246, 0
	v_readlane_b32 s5, v246, 1
	v_readlane_b32 s6, v246, 2
	v_readlane_b32 s7, v246, 3
	v_readlane_b32 s8, v246, 4
	v_readlane_b32 s9, v246, 5
	v_and_b32_e32 v5, 0xc0, v4
	v_and_b32_e32 v3, 15, v4
	v_readlane_b32 s10, v246, 6
	v_readlane_b32 s11, v246, 7
	s_mov_b64 s[4:5], s[8:9]
	s_waitcnt vmcnt(7)
	v_ashrrev_i32_e32 v110, 1, v4
	s_movk_i32 s1, 0xff80
	v_lshrrev_b32_e32 v4, 1, v4
	s_lshl_b64 s[2:3], s[42:43], 13
	s_mov_b64 s[6:7], s[10:11]
	v_and_or_b32 v3, v110, s1, v3
	v_and_b32_e32 v4, 24, v4
	s_add_u32 s4, s6, s2
	v_or3_b32 v4, v5, v4, s0
	v_add_u32_e32 v5, s85, v3
	s_addc_u32 s5, s7, s3
	v_cmp_gt_i32_e32 vcc, s83, v5
	v_ashrrev_i32_e32 v5, 31, v4
	v_lshlrev_b32_e32 v216, 2, v4
	global_load_dwordx4 v[238:241], v216, s[4:5]
	global_load_dwordx4 v[242:245], v216, s[4:5] offset:16
	global_load_dwordx4 v[248:251], v216, s[4:5] offset:128
	global_load_dwordx4 v[252:255], v216, s[4:5] offset:144
	s_waitcnt vmcnt(0) lgkmcnt(0)
	s_barrier
	s_and_saveexec_b64 s[0:1], vcc
	s_cbranch_execz .LBB0_1582
	v_lshl_add_u64 v[118:119], v[4:5], 2, s[4:5]
	v_lshl_add_u32 v120, v3, 3, 0
	v_add_u32_e32 v120, 0x20000, v120
	ds_read_b64 v[120:121], v120
	v_pk_mov_b32 v[122:123], v[166:167], v[168:169] op_sel:[1,0]
	v_pk_mov_b32 v[124:125], v[168:169], v[166:167] op_sel:[1,0]
	s_waitcnt lgkmcnt(0)
	v_ashrrev_i32_e32 v127, 31, v120
	v_mov_b32_e32 v126, v120
	v_lshlrev_b64 v[126:127], 12, v[126:127]
	v_lshl_add_u64 v[126:127], s[22:23], 0, v[126:127]
	v_lshl_add_u64 v[126:127], v[4:5], 1, v[126:127]
	v_pk_add_f32 v[112:113], v[160:161], v[240:241]
	v_pk_add_f32 v[110:111], v[158:159], v[238:239]
	v_pk_add_f32 v[116:117], v[124:125], v[244:245]
	v_pk_add_f32 v[114:115], v[122:123], v[242:243]
	v_pk_mul_f32 v[112:113], v[120:121], v[112:113] op_sel:[1,0]
	v_pk_mul_f32 v[110:111], v[120:121], v[110:111] op_sel:[1,0]
	v_pk_mul_f32 v[116:117], v[120:121], v[116:117] op_sel:[1,0]
	v_pk_mul_f32 v[114:115], v[120:121], v[114:115] op_sel:[1,0]
	v_cvt_pk_bf16_f32 v110, v110, v111
	v_cvt_pk_bf16_f32 v111, v112, v113
	v_cvt_pk_bf16_f32 v112, v114, v115
	v_cvt_pk_bf16_f32 v113, v116, v117
	global_store_dwordx4 v[126:127], v[110:113], off
	s_nop 1
	v_pk_mov_b32 v[118:119], v[154:155], v[156:157] op_sel:[1,0]
	v_pk_mov_b32 v[122:123], v[156:157], v[154:155] op_sel:[1,0]
	v_pk_add_f32 v[112:113], v[152:153], v[250:251]
	v_pk_add_f32 v[110:111], v[150:151], v[248:249]
	v_pk_add_f32 v[116:117], v[122:123], v[254:255]
	v_pk_add_f32 v[114:115], v[118:119], v[252:253]
	v_pk_mul_f32 v[112:113], v[120:121], v[112:113] op_sel:[1,0]
	v_pk_mul_f32 v[110:111], v[120:121], v[110:111] op_sel:[1,0]
	v_pk_mul_f32 v[116:117], v[120:121], v[116:117] op_sel:[1,0]
	v_pk_mul_f32 v[114:115], v[120:121], v[114:115] op_sel:[1,0]
	v_cvt_pk_bf16_f32 v110, v110, v111
	v_cvt_pk_bf16_f32 v111, v112, v113
	v_cvt_pk_bf16_f32 v112, v114, v115
	v_cvt_pk_bf16_f32 v113, v116, v117
	global_store_dwordx4 v[126:127], v[110:113], off offset:64
	s_nop 1
.LBB0_1582:
	s_or_b64 exec, exec, s[0:1]
	s_nop 0
	v_or_b32_e32 v110, 16, v3
	v_add_u32_e32 v111, s85, v110
	v_cmp_gt_i32_e32 vcc, s83, v111
	s_and_saveexec_b64 s[0:1], vcc
	s_cbranch_execz .LBB0_1584
	v_lshl_add_u64 v[120:121], v[4:5], 2, s[4:5]
	v_lshl_add_u32 v110, v110, 3, 0
	v_add_u32_e32 v110, 0x20000, v110
	ds_read_b64 v[122:123], v110
	v_pk_mov_b32 v[110:111], v[146:147], v[148:149] op_sel:[1,0]
	v_pk_mov_b32 v[124:125], v[148:149], v[146:147] op_sel:[1,0]
	s_waitcnt lgkmcnt(0)
	v_ashrrev_i32_e32 v127, 31, v122
	v_mov_b32_e32 v126, v122
	v_lshlrev_b64 v[126:127], 12, v[126:127]
	v_lshl_add_u64 v[126:127], s[22:23], 0, v[126:127]
	v_lshl_add_u64 v[126:127], v[4:5], 1, v[126:127]
	v_pk_add_f32 v[114:115], v[136:137], v[240:241]
	v_pk_add_f32 v[112:113], v[134:135], v[238:239]
	v_pk_add_f32 v[118:119], v[124:125], v[244:245]
	v_pk_add_f32 v[110:111], v[110:111], v[242:243]
	v_pk_mul_f32 v[114:115], v[122:123], v[114:115] op_sel:[1,0]
	v_pk_mul_f32 v[112:113], v[122:123], v[112:113] op_sel:[1,0]
	v_pk_mul_f32 v[116:117], v[122:123], v[118:119] op_sel:[1,0]
	v_pk_mul_f32 v[118:119], v[122:123], v[110:111] op_sel:[1,0]
	v_cvt_pk_bf16_f32 v110, v112, v113
	v_cvt_pk_bf16_f32 v111, v114, v115
	v_cvt_pk_bf16_f32 v112, v118, v119
	v_cvt_pk_bf16_f32 v113, v116, v117
	global_store_dwordx4 v[126:127], v[110:113], off
	s_nop 1
	v_pk_mov_b32 v[118:119], v[106:107], v[108:109] op_sel:[1,0]
	v_pk_mov_b32 v[106:107], v[108:109], v[106:107] op_sel:[1,0]
	v_pk_add_f32 v[104:105], v[104:105], v[250:251]
	v_pk_add_f32 v[102:103], v[102:103], v[248:249]
	v_pk_add_f32 v[106:107], v[106:107], v[254:255]
	v_pk_add_f32 v[108:109], v[118:119], v[252:253]
	v_pk_mul_f32 v[104:105], v[122:123], v[104:105] op_sel:[1,0]
	v_pk_mul_f32 v[102:103], v[122:123], v[102:103] op_sel:[1,0]
	v_pk_mul_f32 v[106:107], v[122:123], v[106:107] op_sel:[1,0]
	v_pk_mul_f32 v[108:109], v[122:123], v[108:109] op_sel:[1,0]
	v_cvt_pk_bf16_f32 v102, v102, v103
	v_cvt_pk_bf16_f32 v103, v104, v105
	v_cvt_pk_bf16_f32 v104, v108, v109
	v_cvt_pk_bf16_f32 v105, v106, v107
	global_store_dwordx4 v[126:127], v[102:105], off offset:64
	s_nop 1
; __device__ __forceinline__ f32x4 rot1(const f32x4 a) { return (f32x4){a[1], a[2], a[3], a[0]}; }
; __device__ __forceinline__ u32x4 pack8(const f32x4 a, const f32x4 b) { u32x4 w; w.x = cvtpk(a[0], a[1]); w.y = cvtpk(a[2], a[3]); w.z = cvtpk(b[0], b[1]); w.w = cvtpk(b[2], b[3]); return w; }
; __device__ __forceinline__ void phase_moe_down(const Ptrs& p, LAS unsigned char* lds) {
;     ...
;         for (int m = 0; m < 8; ++m) { const int rl = T.wr * 128 + m * 16 + T.fr, r = i0 + rl;
;             if (r < mu.cnt) { const int a = tab[2 * rl]; const float gt = __int_as_float(tab[2 * rl + 1]);
; #pragma unroll
;                 for (int pp = 0; pp < 2; ++pp) { const int c = col0 + T.wc * 64 + pp * 32 + T.fq * 8;
;                     const f32x4 v0 = (acc[m][2 * pp] + *(const f32x4*)(bd + c)) * gt, v1 = (rot1(acc[m][2 * pp + 1]) + *(const f32x4*)(bd + c + 4)) * gt;
;                     *(u32x4*)(y + (size_t)a * D + c) = pack8(v0, v1); } } }
.LBB0_1584:
	s_or_b64 exec, exec, s[0:1]
	s_nop 0
	v_or_b32_e32 v102, 32, v3
	v_add_u32_e32 v103, s85, v102
	v_cmp_gt_i32_e32 vcc, s83, v103
	s_and_saveexec_b64 s[0:1], vcc
	s_cbranch_execz .LBB0_1586
	v_lshl_add_u64 v[112:113], v[4:5], 2, s[4:5]
	v_lshl_add_u32 v102, v102, 3, 0
	v_add_u32_e32 v102, 0x20000, v102
	ds_read_b64 v[102:103], v102
	v_pk_mov_b32 v[114:115], v[98:99], v[100:101] op_sel:[1,0]
	v_pk_mov_b32 v[98:99], v[100:101], v[98:99] op_sel:[1,0]
	s_waitcnt lgkmcnt(0)
	v_ashrrev_i32_e32 v101, 31, v102
	v_mov_b32_e32 v100, v102
	v_lshlrev_b64 v[100:101], 12, v[100:101]
	v_lshl_add_u64 v[100:101], s[22:23], 0, v[100:101]
	v_lshl_add_u64 v[116:117], v[4:5], 1, v[100:101]
	v_pk_add_f32 v[96:97], v[96:97], v[240:241]
	v_pk_add_f32 v[94:95], v[94:95], v[238:239]
	v_pk_add_f32 v[98:99], v[98:99], v[244:245]
	v_pk_add_f32 v[100:101], v[114:115], v[242:243]
	v_pk_mul_f32 v[96:97], v[102:103], v[96:97] op_sel:[1,0]
	v_pk_mul_f32 v[94:95], v[102:103], v[94:95] op_sel:[1,0]
	v_pk_mul_f32 v[98:99], v[102:103], v[98:99] op_sel:[1,0]
	v_pk_mul_f32 v[100:101], v[102:103], v[100:101] op_sel:[1,0]
	v_cvt_pk_bf16_f32 v94, v94, v95
	v_cvt_pk_bf16_f32 v95, v96, v97
	v_cvt_pk_bf16_f32 v96, v100, v101
	v_cvt_pk_bf16_f32 v97, v98, v99
	global_store_dwordx4 v[116:117], v[94:97], off
	s_nop 1
	v_pk_mov_b32 v[104:105], v[90:91], v[92:93] op_sel:[1,0]
	v_pk_mov_b32 v[90:91], v[92:93], v[90:91] op_sel:[1,0]
	v_pk_add_f32 v[88:89], v[88:89], v[250:251]
	v_pk_add_f32 v[86:87], v[86:87], v[248:249]
	v_pk_add_f32 v[90:91], v[90:91], v[254:255]
	v_pk_add_f32 v[92:93], v[104:105], v[252:253]
	v_pk_mul_f32 v[88:89], v[102:103], v[88:89] op_sel:[1,0]
	v_pk_mul_f32 v[86:87], v[102:103], v[86:87] op_sel:[1,0]
	v_pk_mul_f32 v[90:91], v[102:103], v[90:91] op_sel:[1,0]
	v_pk_mul_f32 v[92:93], v[102:103], v[92:93] op_sel:[1,0]
	v_cvt_pk_bf16_f32 v86, v86, v87
	v_cvt_pk_bf16_f32 v87, v88, v89
	v_cvt_pk_bf16_f32 v88, v92, v93
	v_cvt_pk_bf16_f32 v89, v90, v91
	global_store_dwordx4 v[116:117], v[86:89], off offset:64
	s_nop 1
.LBB0_1586:
	s_or_b64 exec, exec, s[0:1]
	s_nop 0
	v_or_b32_e32 v86, 48, v3
	v_add_u32_e32 v87, s85, v86
	v_cmp_gt_i32_e32 vcc, s83, v87
	s_and_saveexec_b64 s[0:1], vcc
	s_cbranch_execz .LBB0_1588
	v_lshl_add_u64 v[96:97], v[4:5], 2, s[4:5]
	v_lshl_add_u32 v86, v86, 3, 0
	v_add_u32_e32 v86, 0x20000, v86
	ds_read_b64 v[86:87], v86
	v_pk_mov_b32 v[98:99], v[82:83], v[84:85] op_sel:[1,0]
	v_pk_mov_b32 v[82:83], v[84:85], v[82:83] op_sel:[1,0]
	s_waitcnt lgkmcnt(0)
	v_ashrrev_i32_e32 v85, 31, v86
	v_mov_b32_e32 v84, v86
	v_lshlrev_b64 v[84:85], 12, v[84:85]
	v_lshl_add_u64 v[84:85], s[22:23], 0, v[84:85]
	v_lshl_add_u64 v[100:101], v[4:5], 1, v[84:85]
	v_pk_add_f32 v[80:81], v[80:81], v[240:241]
	v_pk_add_f32 v[78:79], v[78:79], v[238:239]
	v_pk_add_f32 v[82:83], v[82:83], v[244:245]
	v_pk_add_f32 v[84:85], v[98:99], v[242:243]
	v_pk_mul_f32 v[80:81], v[86:87], v[80:81] op_sel:[1,0]
	v_pk_mul_f32 v[78:79], v[86:87], v[78:79] op_sel:[1,0]
	v_pk_mul_f32 v[82:83], v[86:87], v[82:83] op_sel:[1,0]
	v_pk_mul_f32 v[84:85], v[86:87], v[84:85] op_sel:[1,0]
	v_cvt_pk_bf16_f32 v78, v78, v79
	v_cvt_pk_bf16_f32 v79, v80, v81
	v_cvt_pk_bf16_f32 v80, v84, v85
	v_cvt_pk_bf16_f32 v81, v82, v83
	global_store_dwordx4 v[100:101], v[78:81], off
	s_nop 1
	v_pk_mov_b32 v[88:89], v[74:75], v[76:77] op_sel:[1,0]
	v_pk_mov_b32 v[74:75], v[76:77], v[74:75] op_sel:[1,0]
	v_pk_add_f32 v[72:73], v[72:73], v[250:251]
	v_pk_add_f32 v[70:71], v[70:71], v[248:249]
	v_pk_add_f32 v[74:75], v[74:75], v[254:255]
	v_pk_add_f32 v[76:77], v[88:89], v[252:253]
	v_pk_mul_f32 v[72:73], v[86:87], v[72:73] op_sel:[1,0]
	v_pk_mul_f32 v[70:71], v[86:87], v[70:71] op_sel:[1,0]
	v_pk_mul_f32 v[74:75], v[86:87], v[74:75] op_sel:[1,0]
	v_pk_mul_f32 v[76:77], v[86:87], v[76:77] op_sel:[1,0]
	v_cvt_pk_bf16_f32 v70, v70, v71
	v_cvt_pk_bf16_f32 v71, v72, v73
	v_cvt_pk_bf16_f32 v72, v76, v77
	v_cvt_pk_bf16_f32 v73, v74, v75
	global_store_dwordx4 v[100:101], v[70:73], off offset:64
	s_nop 1
.LBB0_1588:
	s_or_b64 exec, exec, s[0:1]
	s_nop 0
	v_or_b32_e32 v70, 64, v3
	v_add_u32_e32 v71, s85, v70
	v_cmp_gt_i32_e32 vcc, s83, v71
	s_and_saveexec_b64 s[0:1], vcc
	s_cbranch_execz .LBB0_1590
	v_lshl_add_u64 v[80:81], v[4:5], 2, s[4:5]
	v_lshl_add_u32 v70, v70, 3, 0
	v_add_u32_e32 v70, 0x20000, v70
	ds_read_b64 v[70:71], v70
	v_pk_mov_b32 v[82:83], v[66:67], v[68:69] op_sel:[1,0]
	v_pk_mov_b32 v[66:67], v[68:69], v[66:67] op_sel:[1,0]
	s_waitcnt lgkmcnt(0)
	v_ashrrev_i32_e32 v69, 31, v70
	v_mov_b32_e32 v68, v70
	v_lshlrev_b64 v[68:69], 12, v[68:69]
	v_lshl_add_u64 v[68:69], s[22:23], 0, v[68:69]
	v_lshl_add_u64 v[84:85], v[4:5], 1, v[68:69]
	v_pk_add_f32 v[64:65], v[64:65], v[240:241]
	v_pk_add_f32 v[62:63], v[62:63], v[238:239]
	v_pk_add_f32 v[66:67], v[66:67], v[244:245]
	v_pk_add_f32 v[68:69], v[82:83], v[242:243]
	v_pk_mul_f32 v[64:65], v[70:71], v[64:65] op_sel:[1,0]
	v_pk_mul_f32 v[62:63], v[70:71], v[62:63] op_sel:[1,0]
	v_pk_mul_f32 v[66:67], v[70:71], v[66:67] op_sel:[1,0]
	v_pk_mul_f32 v[68:69], v[70:71], v[68:69] op_sel:[1,0]
	v_cvt_pk_bf16_f32 v62, v62, v63
	v_cvt_pk_bf16_f32 v63, v64, v65
	v_cvt_pk_bf16_f32 v64, v68, v69
	v_cvt_pk_bf16_f32 v65, v66, v67
	global_store_dwordx4 v[84:85], v[62:65], off
	s_nop 1
	v_pk_mov_b32 v[72:73], v[58:59], v[60:61] op_sel:[1,0]
	v_pk_mov_b32 v[58:59], v[60:61], v[58:59] op_sel:[1,0]
	v_pk_add_f32 v[56:57], v[56:57], v[250:251]
	v_pk_add_f32 v[54:55], v[54:55], v[248:249]
	v_pk_add_f32 v[58:59], v[58:59], v[254:255]
	v_pk_add_f32 v[60:61], v[72:73], v[252:253]
	v_pk_mul_f32 v[56:57], v[70:71], v[56:57] op_sel:[1,0]
	v_pk_mul_f32 v[54:55], v[70:71], v[54:55] op_sel:[1,0]
	v_pk_mul_f32 v[58:59], v[70:71], v[58:59] op_sel:[1,0]
	v_pk_mul_f32 v[60:61], v[70:71], v[60:61] op_sel:[1,0]
	v_cvt_pk_bf16_f32 v54, v54, v55
	v_cvt_pk_bf16_f32 v55, v56, v57
	v_cvt_pk_bf16_f32 v56, v60, v61
	v_cvt_pk_bf16_f32 v57, v58, v59
	global_store_dwordx4 v[84:85], v[54:57], off offset:64
	s_nop 1
; __device__ __forceinline__ f32x4 rot1(const f32x4 a) { return (f32x4){a[1], a[2], a[3], a[0]}; }
; __device__ __forceinline__ u32x4 pack8(const f32x4 a, const f32x4 b) { u32x4 w; w.x = cvtpk(a[0], a[1]); w.y = cvtpk(a[2], a[3]); w.z = cvtpk(b[0], b[1]); w.w = cvtpk(b[2], b[3]); return w; }
; __device__ __forceinline__ void phase_moe_down(const Ptrs& p, LAS unsigned char* lds) {
;     ...
;         for (int m = 0; m < 8; ++m) { const int rl = T.wr * 128 + m * 16 + T.fr, r = i0 + rl;
;             if (r < mu.cnt) { const int a = tab[2 * rl]; const float gt = __int_as_float(tab[2 * rl + 1]);
; #pragma unroll
;                 for (int pp = 0; pp < 2; ++pp) { const int c = col0 + T.wc * 64 + pp * 32 + T.fq * 8;
;                     const f32x4 v0 = (acc[m][2 * pp] + *(const f32x4*)(bd + c)) * gt, v1 = (rot1(acc[m][2 * pp + 1]) + *(const f32x4*)(bd + c + 4)) * gt;
;                     *(u32x4*)(y + (size_t)a * D + c) = pack8(v0, v1); } } }
.LBB0_1590:
	s_or_b64 exec, exec, s[0:1]
	s_nop 0
	v_or_b32_e32 v54, 0x50, v3
	v_add_u32_e32 v55, s85, v54
	v_cmp_gt_i32_e32 vcc, s83, v55
	s_and_saveexec_b64 s[0:1], vcc
	s_cbranch_execz .LBB0_1592
	v_lshl_add_u64 v[64:65], v[4:5], 2, s[4:5]
	v_lshl_add_u32 v54, v54, 3, 0
	v_add_u32_e32 v54, 0x20000, v54
	ds_read_b64 v[54:55], v54
	v_pk_mov_b32 v[66:67], v[50:51], v[52:53] op_sel:[1,0]
	v_pk_mov_b32 v[50:51], v[52:53], v[50:51] op_sel:[1,0]
	s_waitcnt lgkmcnt(0)
	v_ashrrev_i32_e32 v53, 31, v54
	v_mov_b32_e32 v52, v54
	v_lshlrev_b64 v[52:53], 12, v[52:53]
	v_lshl_add_u64 v[52:53], s[22:23], 0, v[52:53]
	v_lshl_add_u64 v[68:69], v[4:5], 1, v[52:53]
	v_pk_add_f32 v[48:49], v[48:49], v[240:241]
	v_pk_add_f32 v[46:47], v[46:47], v[238:239]
	v_pk_add_f32 v[50:51], v[50:51], v[244:245]
	v_pk_add_f32 v[52:53], v[66:67], v[242:243]
	v_pk_mul_f32 v[48:49], v[54:55], v[48:49] op_sel:[1,0]
	v_pk_mul_f32 v[46:47], v[54:55], v[46:47] op_sel:[1,0]
	v_pk_mul_f32 v[50:51], v[54:55], v[50:51] op_sel:[1,0]
	v_pk_mul_f32 v[52:53], v[54:55], v[52:53] op_sel:[1,0]
	v_cvt_pk_bf16_f32 v46, v46, v47
	v_cvt_pk_bf16_f32 v47, v48, v49
	v_cvt_pk_bf16_f32 v48, v52, v53
	v_cvt_pk_bf16_f32 v49, v50, v51
	global_store_dwordx4 v[68:69], v[46:49], off
	s_nop 1
	v_pk_mov_b32 v[56:57], v[42:43], v[44:45] op_sel:[1,0]
	v_pk_mov_b32 v[42:43], v[44:45], v[42:43] op_sel:[1,0]
	v_pk_add_f32 v[40:41], v[40:41], v[250:251]
	v_pk_add_f32 v[38:39], v[38:39], v[248:249]
	v_pk_add_f32 v[42:43], v[42:43], v[254:255]
	v_pk_add_f32 v[44:45], v[56:57], v[252:253]
	v_pk_mul_f32 v[40:41], v[54:55], v[40:41] op_sel:[1,0]
	v_pk_mul_f32 v[38:39], v[54:55], v[38:39] op_sel:[1,0]
	v_pk_mul_f32 v[42:43], v[54:55], v[42:43] op_sel:[1,0]
	v_pk_mul_f32 v[44:45], v[54:55], v[44:45] op_sel:[1,0]
	v_cvt_pk_bf16_f32 v38, v38, v39
	v_cvt_pk_bf16_f32 v39, v40, v41
	v_cvt_pk_bf16_f32 v40, v44, v45
	v_cvt_pk_bf16_f32 v41, v42, v43
	global_store_dwordx4 v[68:69], v[38:41], off offset:64
	s_nop 1
.LBB0_1592:
	s_or_b64 exec, exec, s[0:1]
	s_nop 0
	v_or_b32_e32 v38, 0x60, v3
	v_add_u32_e32 v39, s85, v38
	v_cmp_gt_i32_e32 vcc, s83, v39
	s_and_saveexec_b64 s[0:1], vcc
	s_cbranch_execz .LBB0_1594
	v_lshl_add_u64 v[48:49], v[4:5], 2, s[4:5]
	v_lshl_add_u32 v38, v38, 3, 0
	v_add_u32_e32 v38, 0x20000, v38
	ds_read_b64 v[38:39], v38
	v_pk_mov_b32 v[50:51], v[34:35], v[36:37] op_sel:[1,0]
	v_pk_mov_b32 v[34:35], v[36:37], v[34:35] op_sel:[1,0]
	s_waitcnt lgkmcnt(0)
	v_ashrrev_i32_e32 v37, 31, v38
	v_mov_b32_e32 v36, v38
	v_lshlrev_b64 v[36:37], 12, v[36:37]
	v_lshl_add_u64 v[36:37], s[22:23], 0, v[36:37]
	v_lshl_add_u64 v[52:53], v[4:5], 1, v[36:37]
	v_pk_add_f32 v[32:33], v[32:33], v[240:241]
	v_pk_add_f32 v[30:31], v[30:31], v[238:239]
	v_pk_add_f32 v[34:35], v[34:35], v[244:245]
	v_pk_add_f32 v[36:37], v[50:51], v[242:243]
	v_pk_mul_f32 v[32:33], v[38:39], v[32:33] op_sel:[1,0]
	v_pk_mul_f32 v[30:31], v[38:39], v[30:31] op_sel:[1,0]
	v_pk_mul_f32 v[34:35], v[38:39], v[34:35] op_sel:[1,0]
	v_pk_mul_f32 v[36:37], v[38:39], v[36:37] op_sel:[1,0]
	v_cvt_pk_bf16_f32 v30, v30, v31
	v_cvt_pk_bf16_f32 v31, v32, v33
	v_cvt_pk_bf16_f32 v32, v36, v37
	v_cvt_pk_bf16_f32 v33, v34, v35
	global_store_dwordx4 v[52:53], v[30:33], off
	s_nop 1
	v_pk_mov_b32 v[40:41], v[26:27], v[28:29] op_sel:[1,0]
	v_pk_mov_b32 v[26:27], v[28:29], v[26:27] op_sel:[1,0]
	v_pk_add_f32 v[24:25], v[24:25], v[250:251]
	v_pk_add_f32 v[22:23], v[22:23], v[248:249]
	v_pk_add_f32 v[26:27], v[26:27], v[254:255]
	v_pk_add_f32 v[28:29], v[40:41], v[252:253]
	v_pk_mul_f32 v[24:25], v[38:39], v[24:25] op_sel:[1,0]
	v_pk_mul_f32 v[22:23], v[38:39], v[22:23] op_sel:[1,0]
	v_pk_mul_f32 v[26:27], v[38:39], v[26:27] op_sel:[1,0]
	v_pk_mul_f32 v[28:29], v[38:39], v[28:29] op_sel:[1,0]
	v_cvt_pk_bf16_f32 v22, v22, v23
	v_cvt_pk_bf16_f32 v23, v24, v25
	v_cvt_pk_bf16_f32 v24, v28, v29
	v_cvt_pk_bf16_f32 v25, v26, v27
	global_store_dwordx4 v[52:53], v[22:25], off offset:64
	s_nop 1
.LBB0_1594:
	s_or_b64 exec, exec, s[0:1]
	v_or_b32_e32 v3, 0x70, v3
	v_add_u32_e32 v22, s85, v3
	v_cmp_gt_i32_e32 vcc, s83, v22
	s_and_saveexec_b64 s[0:1], vcc
	s_cbranch_execz .LBB0_1291
	v_lshl_add_u64 v[30:31], v[4:5], 2, s[4:5]
	v_lshl_add_u32 v3, v3, 3, 0
	v_add_u32_e32 v3, 0x20000, v3
	ds_read_b64 v[32:33], v3
	v_pk_mov_b32 v[34:35], v[18:19], v[20:21] op_sel:[1,0]
	v_pk_mov_b32 v[18:19], v[20:21], v[18:19] op_sel:[1,0]
	s_waitcnt lgkmcnt(0)
	v_ashrrev_i32_e32 v21, 31, v32
	v_mov_b32_e32 v20, v32
	v_lshlrev_b64 v[20:21], 12, v[20:21]
	v_lshl_add_u64 v[20:21], s[22:23], 0, v[20:21]
	v_lshl_add_u64 v[36:37], v[4:5], 1, v[20:21]
	v_pk_add_f32 v[4:5], v[16:17], v[240:241]
	v_pk_add_f32 v[14:15], v[14:15], v[238:239]
	v_pk_add_f32 v[16:17], v[18:19], v[244:245]
	v_pk_add_f32 v[18:19], v[34:35], v[242:243]
	v_pk_mul_f32 v[4:5], v[32:33], v[4:5] op_sel:[1,0]
	v_pk_mul_f32 v[14:15], v[32:33], v[14:15] op_sel:[1,0]
	v_pk_mul_f32 v[20:21], v[32:33], v[16:17] op_sel:[1,0]
	v_pk_mul_f32 v[16:17], v[32:33], v[18:19] op_sel:[1,0]
	v_cvt_pk_bf16_f32 v14, v14, v15
	v_cvt_pk_bf16_f32 v15, v4, v5
	v_cvt_pk_bf16_f32 v16, v16, v17
	v_cvt_pk_bf16_f32 v17, v20, v21
	global_store_dwordx4 v[36:37], v[14:17], off
	s_nop 1
	v_pk_mov_b32 v[4:5], v[10:11], v[12:13] op_sel:[1,0]
	v_pk_mov_b32 v[10:11], v[12:13], v[10:11] op_sel:[1,0]
	v_pk_add_f32 v[8:9], v[8:9], v[250:251]
	v_pk_add_f32 v[6:7], v[6:7], v[248:249]
	v_pk_add_f32 v[10:11], v[10:11], v[254:255]
	v_pk_add_f32 v[4:5], v[4:5], v[252:253]
	v_pk_mul_f32 v[8:9], v[32:33], v[8:9] op_sel:[1,0]
	v_pk_mul_f32 v[6:7], v[32:33], v[6:7] op_sel:[1,0]
	v_pk_mul_f32 v[10:11], v[32:33], v[10:11] op_sel:[1,0]
	v_pk_mul_f32 v[12:13], v[32:33], v[4:5] op_sel:[1,0]
	v_cvt_pk_bf16_f32 v4, v6, v7
	v_cvt_pk_bf16_f32 v5, v8, v9
	v_cvt_pk_bf16_f32 v6, v12, v13
	v_cvt_pk_bf16_f32 v7, v10, v11
	global_store_dwordx4 v[36:37], v[4:7], off offset:64
	s_nop 1
	s_branch .LBB0_1291

; __global__ void __launch_bounds__(512, 2) mega_fwd(Ptrs p) {
	.amdhsa_kernel _Z8mega_fwd4Ptrs
		.amdhsa_group_segment_fixed_size 0
		.amdhsa_private_segment_fixed_size 0
		.amdhsa_kernarg_size 440
		.amdhsa_user_sgpr_count 2
		.amdhsa_user_sgpr_dispatch_ptr 0
		.amdhsa_user_sgpr_queue_ptr 0
		.amdhsa_user_sgpr_kernarg_segment_ptr 1
		.amdhsa_user_sgpr_dispatch_id 0
		.amdhsa_user_sgpr_kernarg_preload_length 0
		.amdhsa_user_sgpr_kernarg_preload_offset 0
		.amdhsa_user_sgpr_private_segment_size 0
		.amdhsa_uses_dynamic_stack 0
		.amdhsa_enable_private_segment 0
		.amdhsa_system_sgpr_workgroup_id_x 1
		.amdhsa_system_sgpr_workgroup_id_y 0
		.amdhsa_system_sgpr_workgroup_id_z 0
		.amdhsa_system_sgpr_workgroup_info 0
		.amdhsa_system_vgpr_workitem_id 0
		.amdhsa_next_free_vgpr 256
		.amdhsa_next_free_sgpr 98
		.amdhsa_accum_offset 256
		.amdhsa_reserve_vcc 1
		.amdhsa_float_round_mode_32 0
		.amdhsa_float_round_mode_16_64 0
		.amdhsa_float_denorm_mode_32 3
		.amdhsa_float_denorm_mode_16_64 3
		.amdhsa_dx10_clamp 1
		.amdhsa_ieee_mode 1
		.amdhsa_fp16_overflow 0
		.amdhsa_tg_split 0
		.amdhsa_exception_fp_ieee_invalid_op 0
		.amdhsa_exception_fp_denorm_src 0
		.amdhsa_exception_fp_ieee_div_zero 0
		.amdhsa_exception_fp_ieee_overflow 0
		.amdhsa_exception_fp_ieee_underflow 0
		.amdhsa_exception_fp_ieee_inexact 0
		.amdhsa_exception_int_div_zero 0
	.end_amdhsa_kernel

; __global__ void __launch_bounds__(512, 2) mega_fwd(Ptrs p) {
amdhsa.kernels:
  - .agpr_count:     0
    .args:
      - .offset:         0
        .size:           184
        .value_kind:     by_value
      - .offset:         184
        .size:           4
        .value_kind:     hidden_block_count_x
      - .offset:         188
        .size:           4
        .value_kind:     hidden_block_count_y
      - .offset:         192
        .size:           4
        .value_kind:     hidden_block_count_z
      - .offset:         196
        .size:           2
        .value_kind:     hidden_group_size_x
      - .offset:         198
        .size:           2
        .value_kind:     hidden_group_size_y
      - .offset:         200
        .size:           2
        .value_kind:     hidden_group_size_z
      - .offset:         202
        .size:           2
        .value_kind:     hidden_remainder_x
      - .offset:         204
        .size:           2
        .value_kind:     hidden_remainder_y
      - .offset:         206
        .size:           2
        .value_kind:     hidden_remainder_z
      - .offset:         224
        .size:           8
        .value_kind:     hidden_global_offset_x
      - .offset:         232
        .size:           8
        .value_kind:     hidden_global_offset_y
      - .offset:         240
        .size:           8
        .value_kind:     hidden_global_offset_z
      - .offset:         248
        .size:           2
        .value_kind:     hidden_grid_dims
      - .offset:         304
        .size:           4
        .value_kind:     hidden_dynamic_lds_size
    .group_segment_fixed_size: 0
    .kernarg_segment_align: 8
    .kernarg_segment_size: 440
    .language:       OpenCL C
    .language_version:
      - 2
      - 0
    .max_flat_workgroup_size: 512
    .name:           _Z8mega_fwd4Ptrs
    .private_segment_fixed_size: 0
    .sgpr_count:     104
    .sgpr_spill_count: 28
    .symbol:         _Z8mega_fwd4Ptrs.kd
    .uniform_work_group_size: 1
    .uses_dynamic_stack: false
    .vgpr_count:     256
    .vgpr_spill_count: 0
    .wavefront_size: 64
